# diff epilogue: the xor-1/2/4/8 butterfly steps of the lambda and sub-LN reductions use DPP moves instead of ds_bpermute round trips
# baseline (speedup 1.0000x reference)
; __device__ __forceinline__ int crow(int r, int hi) { return (r & 3) + 8 * (r >> 2) + 4 * hi; }
; __device__ __forceinline__ float wave_sum(float v) {
; #pragma unroll
;     for (int o = 1; o < 64; o <<= 1) v += __shfl_xor(v, o);
;     return v;
; __device__ __forceinline__ void diff_unit(KP Pk, Frame& F, int l, int b, int h, int qrow0, int nkt) {
;     ...
;     if (m == 0) {
;         const float* dl = Pk->in[I_DLAM] + l * 256; const float lam_init = __builtin_bit_cast(float, __builtin_amdgcn_readfirstlane(__builtin_bit_cast(int, l == 0 ? 0.2f : (0.8f - 0.6f * 0.74081822068f))));
;         const float lam = expf(wave_sum(dl[ln_] * dl[64 + ln_])) - expf(wave_sum(dl[128 + ln_] * dl[192 + ln_])) + lam_init;
;         float ssq[16];
; #pragma unroll
;         for (int r = 0; r < 16; ++r) { float a = 0.f;
; #pragma unroll
;             for (int nb = 0; nb < 4; ++nb) { const float v = O[nb][r] * rlr[r] - lam * ex[crow(r, hi) * 128 + nb * 32 + r32]; O[nb][r] = v; a += v * v; }
;             a += __shfl_xor(a, 1); a += __shfl_xor(a, 2); a += __shfl_xor(a, 4); a += __shfl_xor(a, 8); a += __shfl_xor(a, 16);
;             ssq[r] = rsqrtf(a * (1.f / 128.f) + NORM_EPS) * (1.f - lam_init); }
.LBB0_622:
	v_readlane_b32 s26, v253, 17
	v_readlane_b32 s27, v253, 18
	s_andn2_b64 vcc, exec, s[26:27]
	s_waitcnt lgkmcnt(0)
	s_barrier
	s_cbranch_vccnz .LBB0_624
	s_load_dwordx4 s[44:47], s[8:9], 0xd8
	s_lshl_b32 s8, s4, 8
	s_ashr_i32 s9, s8, 31
	s_lshl_b64 s[8:9], s[8:9], 2
	v_ashrrev_i32_e32 v101, 31, v100
	s_waitcnt lgkmcnt(0)
	s_add_u32 s8, s44, s8
	s_addc_u32 s9, s45, s9
	v_lshl_add_u64 v[100:101], v[100:101], 2, s[8:9]
	global_load_dword v69, v[100:101], off
	global_load_dword v71, v[100:101], off offset:256
	global_load_dword v250, v[100:101], off offset:512
	global_load_dword v251, v[100:101], off offset:768
	s_cmp_eq_u32 s4, 0
	s_mov_b32 s5, 0x3e4ccccd
	s_cselect_b32 s5, s5, 0x3eb60549
	v_mov_b32_e32 v102, v2
	v_mov_b32_e32 v103, v18
	v_mov_b32_e32 v146, v50
	v_mov_b32_e32 v147, v34
	v_mov_b32_e32 v18, v3
	v_mov_b32_e32 v50, v35
	s_mov_b32 s8, 0x358637bd
	v_mov_b32_e32 v106, s46
	v_mov_b32_e32 v107, s47
	s_mov_b32 s41, s61
	v_mov_b32_e32 v105, v0
	v_ashrrev_i32_e32 v93, 31, v92
	v_lshlrev_b64 v[92:93], 11, v[92:93]
	v_ashrrev_i32_e32 v91, 31, v90
	v_lshlrev_b64 v[90:91], 11, v[90:91]
	v_ashrrev_i32_e32 v89, 31, v88
	v_lshlrev_b64 v[88:89], 11, v[88:89]
	v_ashrrev_i32_e32 v87, 31, v86
	v_lshlrev_b64 v[86:87], 11, v[86:87]
	v_ashrrev_i32_e32 v85, 31, v84
	v_lshlrev_b64 v[84:85], 11, v[84:85]
	v_ashrrev_i32_e32 v83, 31, v82
	v_lshlrev_b64 v[82:83], 11, v[82:83]
	v_ashrrev_i32_e32 v81, 31, v80
	v_lshlrev_b64 v[80:81], 11, v[80:81]
	v_ashrrev_i32_e32 v79, 31, v78
	v_lshlrev_b64 v[78:79], 11, v[78:79]
	v_ashrrev_i32_e32 v99, 31, v98
	v_ashrrev_i32_e32 v97, 31, v96
	v_ashrrev_i32_e32 v95, 31, v94
	v_lshlrev_b64 v[94:95], 11, v[94:95]
	s_waitcnt vmcnt(0)
	v_mul_f32_e32 v73, v69, v71
	s_nop 1
	v_mov_b32_dpp v73, v73 quad_perm:[1,0,3,2] row_mask:0xf bank_mask:0xf
	s_waitcnt lgkmcnt(0)
	v_fmac_f32_e32 v73, v69, v71
	s_nop 1
	v_mov_b32_dpp v69, v73 quad_perm:[2,3,0,1] row_mask:0xf bank_mask:0xf
	s_waitcnt lgkmcnt(0)
	v_add_f32_e32 v69, v73, v69
	s_nop 1
	v_mov_b32_dpp v71, v69 row_half_mirror row_mask:0xf bank_mask:0xf
	s_waitcnt lgkmcnt(0)
	v_add_f32_e32 v69, v69, v71
	s_nop 1
	v_mov_b32_dpp v71, v69 row_mirror row_mask:0xf bank_mask:0xf
	s_waitcnt lgkmcnt(0)
	v_add_f32_e32 v69, v69, v71
	ds_bpermute_b32 v71, v1, v69
	s_waitcnt lgkmcnt(0)
	v_add_f32_e32 v69, v69, v71
	ds_bpermute_b32 v71, v143, v69
	s_waitcnt lgkmcnt(0)
	v_add_f32_e32 v69, v69, v71
	v_mul_f32_e32 v71, 0x3fb8aa3b, v69
	v_fma_f32 v73, v69, s10, -v71
	v_rndne_f32_e32 v75, v71
	v_fmac_f32_e32 v73, 0x32a5705f, v69
	v_sub_f32_e32 v71, v71, v75
	v_add_f32_e32 v71, v71, v73
	v_exp_f32_e32 v71, v71
	v_cvt_i32_f32_e32 v73, v75
	v_cmp_ngt_f32_e32 vcc, s11, v69
	v_ldexp_f32 v71, v71, v73
	s_nop 0
	v_cndmask_b32_e32 v71, 0, v71, vcc
	v_cmp_nlt_f32_e32 vcc, s12, v69
	s_nop 1
	v_cndmask_b32_e32 v69, v237, v71, vcc
	v_mov_b32_e32 v71, v250
	v_mov_b32_e32 v73, v251
	ds_read2_b32 v[100:101], v67 offset1:32
	v_mul_f32_e32 v75, v71, v73
	s_nop 1
	v_mov_b32_dpp v75, v75 quad_perm:[1,0,3,2] row_mask:0xf bank_mask:0xf
	s_waitcnt lgkmcnt(0)
	v_fmac_f32_e32 v75, v71, v73
	s_nop 1
	v_mov_b32_dpp v71, v75 quad_perm:[2,3,0,1] row_mask:0xf bank_mask:0xf
	s_waitcnt lgkmcnt(0)
	v_add_f32_e32 v71, v75, v71
	s_nop 1
	v_mov_b32_dpp v73, v71 row_half_mirror row_mask:0xf bank_mask:0xf
	s_waitcnt lgkmcnt(0)
	v_add_f32_e32 v71, v71, v73
	s_nop 1
	v_mov_b32_dpp v73, v71 row_mirror row_mask:0xf bank_mask:0xf
	s_waitcnt lgkmcnt(0)
	v_add_f32_e32 v71, v71, v73
	ds_bpermute_b32 v73, v1, v71
	s_waitcnt lgkmcnt(0)
	v_add_f32_e32 v71, v71, v73
	ds_bpermute_b32 v73, v143, v71
	s_waitcnt lgkmcnt(0)
	v_add_f32_e32 v71, v71, v73
	v_mul_f32_e32 v73, 0x3fb8aa3b, v71
	v_fma_f32 v75, v71, s10, -v73
	v_rndne_f32_e32 v77, v73
	v_fmac_f32_e32 v75, 0x32a5705f, v71
	v_sub_f32_e32 v73, v73, v77
	v_add_f32_e32 v73, v73, v75
	v_exp_f32_e32 v73, v73
	v_cvt_i32_f32_e32 v75, v77
	v_cmp_ngt_f32_e32 vcc, s11, v71
	v_ldexp_f32 v73, v73, v75
	s_nop 0
	v_cndmask_b32_e32 v73, 0, v73, vcc
	v_cmp_nlt_f32_e32 vcc, s12, v71
	v_ashrrev_i32_e32 v75, 31, v74
	v_lshlrev_b64 v[74:75], 11, v[74:75]
	v_cndmask_b32_e32 v71, v237, v73, vcc
	v_sub_f32_e32 v69, v69, v71
	v_add_f32_e32 v116, s5, v69
	v_pk_mul_f32 v[100:101], v[100:101], v[116:117] op_sel_hi:[1,0]
	v_sub_f32_e64 v69, 1.0, s5
	v_pk_fma_f32 v[100:101], v[102:103], v[76:77], v[100:101] op_sel_hi:[1,0,1] neg_lo:[0,0,1] neg_hi:[0,0,1]
	ds_read2_b32 v[102:103], v67 offset0:64 offset1:96
	v_pk_mul_f32 v[144:145], v[100:101], v[100:101]
	v_add_u32_e32 v71, 0x400, v67
	v_readlane_b32 s5, v254, 61
	v_ashrrev_i32_e32 v73, 31, v72
	s_waitcnt lgkmcnt(0)
	v_mov_b32_e32 v148, v103
	v_mov_b32_e32 v149, v102
	v_pk_mul_f32 v[102:103], v[116:117], v[148:149] op_sel_hi:[0,1]
	v_pk_fma_f32 v[76:77], v[146:147], v[76:77], v[102:103] op_sel_hi:[1,0,1] neg_lo:[0,0,1] neg_hi:[0,0,1]
	ds_read2_b32 v[102:103], v67 offset0:128 offset1:160
	v_pk_mul_f32 v[146:147], v[76:77], v[76:77]
	v_lshlrev_b64 v[72:73], 11, v[72:73]
	s_waitcnt lgkmcnt(0)
	v_pk_mul_f32 v[2:3], v[116:117], v[102:103] op_sel_hi:[0,1]
	v_pk_fma_f32 v[102:103], v[18:19], v[122:123], v[2:3] op_sel_hi:[1,0,1] neg_lo:[0,0,1] neg_hi:[0,0,1]
	ds_read2_b32 v[2:3], v67 offset0:192 offset1:224
	v_pk_mul_f32 v[18:19], v[102:103], v[102:103]
	s_waitcnt lgkmcnt(0)
; __device__ __forceinline__ int crow(int r, int hi) { return (r & 3) + 8 * (r >> 2) + 4 * hi; }
; __device__ __forceinline__ void diff_unit(KP Pk, Frame& F, int l, int b, int h, int qrow0, int nkt) {
;     ...
;         float ssq[16];
; #pragma unroll
;         for (int r = 0; r < 16; ++r) { float a = 0.f;
; #pragma unroll
;             for (int nb = 0; nb < 4; ++nb) { const float v = O[nb][r] * rlr[r] - lam * ex[crow(r, hi) * 128 + nb * 32 + r32]; O[nb][r] = v; a += v * v; }
;             a += __shfl_xor(a, 1); a += __shfl_xor(a, 2); a += __shfl_xor(a, 4); a += __shfl_xor(a, 8); a += __shfl_xor(a, 16);
;             ssq[r] = rsqrtf(a * (1.f / 128.f) + NORM_EPS) * (1.f - lam_init); }
	v_pk_mul_f32 v[2:3], v[116:117], v[2:3] op_sel_hi:[0,1]
	v_pk_fma_f32 v[2:3], v[50:51], v[122:123], v[2:3] op_sel_hi:[1,0,1] neg_lo:[0,0,1] neg_hi:[0,0,1]
	v_mov_b32_e32 v50, v18
	v_pk_mul_f32 v[34:35], v[2:3], v[2:3]
	v_mov_b32_e32 v51, v144
	v_mov_b32_e32 v144, v19
	v_pk_add_f32 v[18:19], v[50:51], v[144:145]
	v_mov_b32_e32 v50, v34
	v_mov_b32_e32 v51, v147
	v_pk_add_f32 v[18:19], v[18:19], v[50:51]
	v_pk_mov_b32 v[34:35], v[34:35], v[146:147] op_sel:[1,0]
	v_mov_b64_e32 v[122:123], s[8:9]
	v_pk_add_f32 v[18:19], v[18:19], v[34:35]
	s_nop 1
	v_mov_b32_dpp v35, v19 quad_perm:[1,0,3,2] row_mask:0xf bank_mask:0xf
	v_mov_b32_dpp v34, v18 quad_perm:[1,0,3,2] row_mask:0xf bank_mask:0xf
	s_brev_b32 s8, 60
	ds_read2_b32 v[146:147], v71 offset0:128 offset1:160
	v_mov_b32_e32 v144, v36
	v_mov_b32_e32 v145, v52
	s_waitcnt lgkmcnt(0)
	v_pk_add_f32 v[18:19], v[18:19], v[34:35]
	s_nop 1
	v_mov_b32_dpp v35, v19 quad_perm:[2,3,0,1] row_mask:0xf bank_mask:0xf
	v_mov_b32_dpp v34, v18 quad_perm:[2,3,0,1] row_mask:0xf bank_mask:0xf
	v_mov_b32_e32 v52, v37
	s_waitcnt lgkmcnt(0)
	v_pk_add_f32 v[18:19], v[18:19], v[34:35]
	s_nop 1
	v_mov_b32_dpp v35, v19 row_half_mirror row_mask:0xf bank_mask:0xf
	v_mov_b32_dpp v34, v18 row_half_mirror row_mask:0xf bank_mask:0xf
	s_waitcnt lgkmcnt(0)
	v_pk_add_f32 v[18:19], v[18:19], v[34:35]
	s_nop 1
	v_mov_b32_dpp v35, v19 row_mirror row_mask:0xf bank_mask:0xf
	v_mov_b32_dpp v34, v18 row_mirror row_mask:0xf bank_mask:0xf
	s_waitcnt lgkmcnt(0)
	v_pk_add_f32 v[18:19], v[18:19], v[34:35]
	ds_bpermute_b32 v35, v1, v19
	ds_bpermute_b32 v34, v1, v18
	s_waitcnt lgkmcnt(0)
	v_pk_add_f32 v[18:19], v[18:19], v[34:35]
	s_nop 0
	v_pk_fma_f32 v[18:19], v[18:19], s[8:9], v[122:123] op_sel_hi:[1,0,0]
	v_mov_b32_e32 v35, v20
	v_mul_f32_e32 v34, 0x4b800000, v19
	v_cmp_gt_f32_e64 s[38:39], s66, v19
	v_cmp_gt_f32_e32 vcc, s66, v18
	v_mov_b32_e32 v20, v5
	v_cndmask_b32_e64 v19, v19, v34, s[38:39]
	v_rsq_f32_e32 v19, v19
	s_nop 0
	v_mul_f32_e32 v34, 0x45800000, v19
	v_cndmask_b32_e64 v19, v19, v34, s[38:39]
	v_mul_f32_e32 v111, v69, v19
	v_mul_f32_e32 v19, 0x4b800000, v18
	v_cndmask_b32_e32 v18, v18, v19, vcc
	v_rsq_f32_e32 v18, v18
	v_mov_b32_e32 v34, v4
	v_pk_mul_f32 v[4:5], v[116:117], v[146:147] op_sel_hi:[0,1]
	v_pk_fma_f32 v[20:21], v[20:21], v[136:137], v[4:5] op_sel_hi:[1,0,1] neg_lo:[0,0,1] neg_hi:[0,0,1]
	v_mul_f32_e32 v19, 0x45800000, v18
	v_cndmask_b32_e32 v18, v18, v19, vcc
	v_mul_f32_e32 v109, v69, v18
	ds_read2_b32 v[18:19], v71 offset1:32
	ds_read2_b32 v[4:5], v71 offset0:192 offset1:224
	v_pk_mul_f32 v[146:147], v[20:21], v[20:21]
	v_mul_f32_e32 v2, v2, v109
	v_mul_f32_e32 v3, v3, v109
	s_waitcnt lgkmcnt(0)
	v_pk_mul_f32 v[18:19], v[116:117], v[18:19] op_sel_hi:[0,1]
	v_pk_fma_f32 v[34:35], v[34:35], v[138:139], v[18:19] op_sel_hi:[1,0,1] neg_lo:[0,0,1] neg_hi:[0,0,1]
	ds_read2_b32 v[18:19], v71 offset0:64 offset1:96
	s_waitcnt lgkmcnt(0)
	v_pk_mul_f32 v[4:5], v[116:117], v[4:5] op_sel_hi:[0,1]
	v_pk_mul_f32 v[50:51], v[34:35], v[34:35]
	v_pk_fma_f32 v[4:5], v[52:53], v[136:137], v[4:5] op_sel_hi:[1,0,1] neg_lo:[0,0,1] neg_hi:[0,0,1]
	v_mov_b32_e32 v52, v146
	s_waitcnt lgkmcnt(0)
	v_pk_mul_f32 v[18:19], v[116:117], v[18:19] op_sel_hi:[0,1]
	v_pk_fma_f32 v[18:19], v[144:145], v[138:139], v[18:19] op_sel_hi:[1,0,1] neg_lo:[0,0,1] neg_hi:[0,0,1]
	v_pk_mul_f32 v[36:37], v[4:5], v[4:5]
	v_pk_mul_f32 v[144:145], v[18:19], v[18:19]
	v_mov_b32_e32 v53, v50
	v_mov_b32_e32 v50, v147
	v_pk_add_f32 v[50:51], v[52:53], v[50:51]
	v_mov_b32_e32 v52, v36
	v_mov_b32_e32 v53, v144
	v_pk_add_f32 v[50:51], v[50:51], v[52:53]
	v_mov_b32_e32 v144, v37
	v_pk_add_f32 v[36:37], v[50:51], v[144:145]
	s_nop 1
	v_mov_b32_dpp v51, v37 quad_perm:[1,0,3,2] row_mask:0xf bank_mask:0xf
	v_mov_b32_dpp v50, v36 quad_perm:[1,0,3,2] row_mask:0xf bank_mask:0xf
	v_add_u32_e32 v71, 0x1000, v67
	v_mov_b32_e32 v52, v38
	v_mov_b32_e32 v53, v54
	v_mov_b32_e32 v54, v39
	s_waitcnt lgkmcnt(0)
	v_pk_add_f32 v[36:37], v[36:37], v[50:51]
	s_nop 1
	v_mov_b32_dpp v51, v37 quad_perm:[2,3,0,1] row_mask:0xf bank_mask:0xf
	v_mov_b32_dpp v50, v36 quad_perm:[2,3,0,1] row_mask:0xf bank_mask:0xf
	s_waitcnt lgkmcnt(0)
	v_pk_add_f32 v[36:37], v[36:37], v[50:51]
	s_nop 1
	v_mov_b32_dpp v51, v37 row_half_mirror row_mask:0xf bank_mask:0xf
	v_mov_b32_dpp v50, v36 row_half_mirror row_mask:0xf bank_mask:0xf
	s_waitcnt lgkmcnt(0)
	v_pk_add_f32 v[36:37], v[36:37], v[50:51]
	s_nop 1
	v_mov_b32_dpp v51, v37 row_mirror row_mask:0xf bank_mask:0xf
	v_mov_b32_dpp v50, v36 row_mirror row_mask:0xf bank_mask:0xf
	s_waitcnt lgkmcnt(0)
	v_pk_add_f32 v[36:37], v[36:37], v[50:51]
	ds_bpermute_b32 v51, v1, v37
	ds_bpermute_b32 v50, v1, v36
	s_waitcnt lgkmcnt(0)
	v_pk_add_f32 v[36:37], v[36:37], v[50:51]
	s_nop 0
	v_pk_fma_f32 v[36:37], v[36:37], s[8:9], v[122:123] op_sel_hi:[1,0,0]
	v_mov_b32_e32 v51, v22
	v_mul_f32_e32 v50, 0x4b800000, v37
	v_cmp_gt_f32_e64 s[38:39], s66, v37
	v_cmp_gt_f32_e32 vcc, s66, v36
	v_mov_b32_e32 v22, v7
	v_cndmask_b32_e64 v37, v37, v50, s[38:39]
	v_rsq_f32_e32 v37, v37
	s_nop 0
	v_mul_f32_e32 v50, 0x45800000, v37
	v_cndmask_b32_e64 v37, v37, v50, s[38:39]
	v_mul_f32_e32 v115, v69, v37
	v_mul_f32_e32 v37, 0x4b800000, v36
	v_cndmask_b32_e32 v36, v36, v37, vcc
	v_rsq_f32_e32 v36, v36
	v_mov_b32_e32 v50, v6
	v_mul_f32_e32 v34, v34, v115
	v_mul_f32_e32 v37, 0x45800000, v36
	v_cndmask_b32_e32 v36, v36, v37, vcc
	v_mul_f32_e32 v113, v69, v36
	ds_read2_b32 v[36:37], v71 offset1:32
	v_mul_f32_e32 v20, v20, v113
	v_mul_f32_e32 v21, v21, v113
	s_waitcnt lgkmcnt(0)
; __device__ __forceinline__ int crow(int r, int hi) { return (r & 3) + 8 * (r >> 2) + 4 * hi; }
; __device__ __forceinline__ void diff_unit(KP Pk, Frame& F, int l, int b, int h, int qrow0, int nkt) {
;     ...
;         float ssq[16];
; #pragma unroll
;         for (int r = 0; r < 16; ++r) { float a = 0.f;
; #pragma unroll
;             for (int nb = 0; nb < 4; ++nb) { const float v = O[nb][r] * rlr[r] - lam * ex[crow(r, hi) * 128 + nb * 32 + r32]; O[nb][r] = v; a += v * v; }
;             a += __shfl_xor(a, 1); a += __shfl_xor(a, 2); a += __shfl_xor(a, 4); a += __shfl_xor(a, 8); a += __shfl_xor(a, 16);
;             ssq[r] = rsqrtf(a * (1.f / 128.f) + NORM_EPS) * (1.f - lam_init); }
	v_pk_mul_f32 v[36:37], v[116:117], v[36:37] op_sel_hi:[0,1]
	v_pk_fma_f32 v[36:37], v[50:51], v[134:135], v[36:37] op_sel_hi:[1,0,1] neg_lo:[0,0,1] neg_hi:[0,0,1]
	ds_read2_b32 v[50:51], v71 offset0:64 offset1:96
	v_pk_mul_f32 v[136:137], v[36:37], v[36:37]
	s_waitcnt lgkmcnt(0)
	v_pk_mul_f32 v[50:51], v[116:117], v[50:51] op_sel_hi:[0,1]
	v_pk_fma_f32 v[50:51], v[52:53], v[134:135], v[50:51] op_sel_hi:[1,0,1] neg_lo:[0,0,1] neg_hi:[0,0,1]
	ds_read2_b32 v[52:53], v71 offset0:128 offset1:160
	v_pk_mul_f32 v[134:135], v[50:51], v[50:51]
	s_waitcnt lgkmcnt(0)
	v_pk_mul_f32 v[6:7], v[116:117], v[52:53] op_sel_hi:[0,1]
	v_pk_fma_f32 v[52:53], v[22:23], v[132:133], v[6:7] op_sel_hi:[1,0,1] neg_lo:[0,0,1] neg_hi:[0,0,1]
	ds_read2_b32 v[6:7], v71 offset0:192 offset1:224
	v_pk_mul_f32 v[22:23], v[52:53], v[52:53]
	v_add_u32_e32 v71, 0x1400, v67
	s_waitcnt lgkmcnt(0)
	v_pk_mul_f32 v[6:7], v[116:117], v[6:7] op_sel_hi:[0,1]
	v_pk_fma_f32 v[6:7], v[54:55], v[132:133], v[6:7] op_sel_hi:[1,0,1] neg_lo:[0,0,1] neg_hi:[0,0,1]
	v_mov_b32_e32 v54, v22
	v_pk_mul_f32 v[38:39], v[6:7], v[6:7]
	v_mov_b32_e32 v55, v136
	v_mov_b32_e32 v136, v23
	v_pk_add_f32 v[22:23], v[54:55], v[136:137]
	v_mov_b32_e32 v54, v38
	v_mov_b32_e32 v55, v134
	v_pk_add_f32 v[22:23], v[22:23], v[54:55]
	v_mov_b32_e32 v134, v39
	v_pk_add_f32 v[22:23], v[22:23], v[134:135]
	s_nop 1
	v_mov_b32_dpp v39, v23 quad_perm:[1,0,3,2] row_mask:0xf bank_mask:0xf
	v_mov_b32_dpp v38, v22 quad_perm:[1,0,3,2] row_mask:0xf bank_mask:0xf
	v_mov_b32_e32 v54, v40
	v_mov_b32_e32 v55, v56
	v_mov_b32_e32 v56, v41
	s_waitcnt lgkmcnt(0)
	v_pk_add_f32 v[22:23], v[22:23], v[38:39]
	s_nop 1
	v_mov_b32_dpp v39, v23 quad_perm:[2,3,0,1] row_mask:0xf bank_mask:0xf
	v_mov_b32_dpp v38, v22 quad_perm:[2,3,0,1] row_mask:0xf bank_mask:0xf
	s_waitcnt lgkmcnt(0)
	v_pk_add_f32 v[22:23], v[22:23], v[38:39]
	s_nop 1
	v_mov_b32_dpp v39, v23 row_half_mirror row_mask:0xf bank_mask:0xf
	v_mov_b32_dpp v38, v22 row_half_mirror row_mask:0xf bank_mask:0xf
	s_waitcnt lgkmcnt(0)
	v_pk_add_f32 v[22:23], v[22:23], v[38:39]
	s_nop 1
	v_mov_b32_dpp v39, v23 row_mirror row_mask:0xf bank_mask:0xf
	v_mov_b32_dpp v38, v22 row_mirror row_mask:0xf bank_mask:0xf
	s_waitcnt lgkmcnt(0)
	v_pk_add_f32 v[22:23], v[22:23], v[38:39]
	ds_bpermute_b32 v39, v1, v23
	ds_bpermute_b32 v38, v1, v22
	s_waitcnt lgkmcnt(0)
	v_pk_add_f32 v[22:23], v[22:23], v[38:39]
	s_nop 0
	v_pk_fma_f32 v[22:23], v[22:23], s[8:9], v[122:123] op_sel_hi:[1,0,0]
	v_mov_b32_e32 v39, v24
	v_mul_f32_e32 v38, 0x4b800000, v23
	v_cmp_gt_f32_e64 s[38:39], s66, v23
	v_cmp_gt_f32_e32 vcc, s66, v22
	v_mov_b32_e32 v24, v9
	v_cndmask_b32_e64 v23, v23, v38, s[38:39]
	v_rsq_f32_e32 v23, v23
	s_nop 0
	v_mul_f32_e32 v38, 0x45800000, v23
	v_cndmask_b32_e64 v23, v23, v38, s[38:39]
	v_mul_f32_e32 v119, v69, v23
	v_mul_f32_e32 v23, 0x4b800000, v22
	v_cndmask_b32_e32 v22, v22, v23, vcc
	v_rsq_f32_e32 v22, v22
	v_mov_b32_e32 v38, v8
	v_mul_f32_e32 v23, 0x45800000, v22
	v_cndmask_b32_e32 v22, v22, v23, vcc
	v_mul_f32_e32 v117, v69, v22
	ds_read2_b32 v[22:23], v71 offset1:32
	s_waitcnt lgkmcnt(0)
	v_pk_mul_f32 v[22:23], v[116:117], v[22:23] op_sel_hi:[0,1]
	v_pk_fma_f32 v[38:39], v[38:39], v[130:131], v[22:23] op_sel_hi:[1,0,1] neg_lo:[0,0,1] neg_hi:[0,0,1]
	ds_read2_b32 v[22:23], v71 offset0:64 offset1:96
	v_pk_mul_f32 v[132:133], v[38:39], v[38:39]
	s_waitcnt lgkmcnt(0)
	v_pk_mul_f32 v[22:23], v[116:117], v[22:23] op_sel_hi:[0,1]
	v_pk_fma_f32 v[22:23], v[54:55], v[130:131], v[22:23] op_sel_hi:[1,0,1] neg_lo:[0,0,1] neg_hi:[0,0,1]
	ds_read2_b32 v[54:55], v71 offset0:128 offset1:160
	v_pk_mul_f32 v[130:131], v[22:23], v[22:23]
	s_waitcnt lgkmcnt(0)
	v_pk_mul_f32 v[8:9], v[116:117], v[54:55] op_sel_hi:[0,1]
	v_pk_fma_f32 v[54:55], v[24:25], v[128:129], v[8:9] op_sel_hi:[1,0,1] neg_lo:[0,0,1] neg_hi:[0,0,1]
	ds_read2_b32 v[8:9], v71 offset0:192 offset1:224
	v_pk_mul_f32 v[24:25], v[54:55], v[54:55]
	v_add_u32_e32 v71, 0x2000, v67
	s_waitcnt lgkmcnt(0)
	v_pk_mul_f32 v[8:9], v[116:117], v[8:9] op_sel_hi:[0,1]
	v_pk_fma_f32 v[8:9], v[56:57], v[128:129], v[8:9] op_sel_hi:[1,0,1] neg_lo:[0,0,1] neg_hi:[0,0,1]
	v_mov_b32_e32 v56, v24
	v_pk_mul_f32 v[40:41], v[8:9], v[8:9]
	v_mov_b32_e32 v57, v132
	v_mov_b32_e32 v132, v25
	v_pk_add_f32 v[24:25], v[56:57], v[132:133]
	v_mov_b32_e32 v56, v40
	v_mov_b32_e32 v57, v130
	v_pk_add_f32 v[24:25], v[24:25], v[56:57]
	v_mov_b32_e32 v130, v41
	v_pk_add_f32 v[24:25], v[24:25], v[130:131]
	s_nop 1
	v_mov_b32_dpp v41, v25 quad_perm:[1,0,3,2] row_mask:0xf bank_mask:0xf
	v_mov_b32_dpp v40, v24 quad_perm:[1,0,3,2] row_mask:0xf bank_mask:0xf
	v_mov_b32_e32 v56, v42
	v_mov_b32_e32 v57, v58
	v_mov_b32_e32 v58, v43
	s_waitcnt lgkmcnt(0)
	v_pk_add_f32 v[24:25], v[24:25], v[40:41]
	s_nop 1
	v_mov_b32_dpp v41, v25 quad_perm:[2,3,0,1] row_mask:0xf bank_mask:0xf
	v_mov_b32_dpp v40, v24 quad_perm:[2,3,0,1] row_mask:0xf bank_mask:0xf
	s_waitcnt lgkmcnt(0)
	v_pk_add_f32 v[24:25], v[24:25], v[40:41]
	s_nop 1
	v_mov_b32_dpp v41, v25 row_half_mirror row_mask:0xf bank_mask:0xf
	v_mov_b32_dpp v40, v24 row_half_mirror row_mask:0xf bank_mask:0xf
	s_waitcnt lgkmcnt(0)
	v_pk_add_f32 v[24:25], v[24:25], v[40:41]
	s_nop 1
	v_mov_b32_dpp v41, v25 row_mirror row_mask:0xf bank_mask:0xf
	v_mov_b32_dpp v40, v24 row_mirror row_mask:0xf bank_mask:0xf
	s_waitcnt lgkmcnt(0)
	v_pk_add_f32 v[24:25], v[24:25], v[40:41]
	ds_bpermute_b32 v41, v1, v25
	ds_bpermute_b32 v40, v1, v24
	s_waitcnt lgkmcnt(0)
; __device__ __forceinline__ int crow(int r, int hi) { return (r & 3) + 8 * (r >> 2) + 4 * hi; }
; __device__ __forceinline__ void diff_unit(KP Pk, Frame& F, int l, int b, int h, int qrow0, int nkt) {
;     ...
;         float ssq[16];
; #pragma unroll
;         for (int r = 0; r < 16; ++r) { float a = 0.f;
; #pragma unroll
;             for (int nb = 0; nb < 4; ++nb) { const float v = O[nb][r] * rlr[r] - lam * ex[crow(r, hi) * 128 + nb * 32 + r32]; O[nb][r] = v; a += v * v; }
;             a += __shfl_xor(a, 1); a += __shfl_xor(a, 2); a += __shfl_xor(a, 4); a += __shfl_xor(a, 8); a += __shfl_xor(a, 16);
;             ssq[r] = rsqrtf(a * (1.f / 128.f) + NORM_EPS) * (1.f - lam_init); }
	v_pk_add_f32 v[24:25], v[24:25], v[40:41]
	s_nop 0
	v_pk_fma_f32 v[24:25], v[24:25], s[8:9], v[122:123] op_sel_hi:[1,0,0]
	v_mov_b32_e32 v41, v26
	v_mul_f32_e32 v40, 0x4b800000, v25
	v_cmp_gt_f32_e64 s[38:39], s66, v25
	v_cmp_gt_f32_e32 vcc, s66, v24
	v_mov_b32_e32 v26, v11
	v_cndmask_b32_e64 v25, v25, v40, s[38:39]
	v_rsq_f32_e32 v25, v25
	s_nop 0
	v_mul_f32_e32 v40, 0x45800000, v25
	v_cndmask_b32_e64 v25, v25, v40, s[38:39]
	v_mul_f32_e32 v125, v69, v25
	v_mul_f32_e32 v25, 0x4b800000, v24
	v_cndmask_b32_e32 v24, v24, v25, vcc
	v_rsq_f32_e32 v24, v24
	v_mov_b32_e32 v40, v10
	v_mul_f32_e32 v25, 0x45800000, v24
	v_cndmask_b32_e32 v24, v24, v25, vcc
	v_mul_f32_e32 v121, v69, v24
	ds_read2_b32 v[24:25], v71 offset1:32
	s_waitcnt lgkmcnt(0)
	v_pk_mul_f32 v[24:25], v[116:117], v[24:25] op_sel_hi:[0,1]
	v_pk_fma_f32 v[40:41], v[40:41], v[126:127], v[24:25] op_sel_hi:[1,0,1] neg_lo:[0,0,1] neg_hi:[0,0,1]
	ds_read2_b32 v[24:25], v71 offset0:64 offset1:96
	v_pk_mul_f32 v[128:129], v[40:41], v[40:41]
	s_waitcnt lgkmcnt(0)
	v_pk_mul_f32 v[24:25], v[116:117], v[24:25] op_sel_hi:[0,1]
	v_pk_fma_f32 v[24:25], v[56:57], v[126:127], v[24:25] op_sel_hi:[1,0,1] neg_lo:[0,0,1] neg_hi:[0,0,1]
	ds_read2_b32 v[56:57], v71 offset0:128 offset1:160
	v_pk_mul_f32 v[126:127], v[24:25], v[24:25]
	s_waitcnt lgkmcnt(0)
	v_pk_mul_f32 v[10:11], v[116:117], v[56:57] op_sel_hi:[0,1]
	v_pk_fma_f32 v[56:57], v[26:27], v[124:125], v[10:11] op_sel_hi:[1,0,1] neg_lo:[0,0,1] neg_hi:[0,0,1]
	ds_read2_b32 v[10:11], v71 offset0:192 offset1:224
	v_pk_mul_f32 v[26:27], v[56:57], v[56:57]
	v_add_u32_e32 v71, 0x2400, v67
	s_waitcnt lgkmcnt(0)
	v_pk_mul_f32 v[10:11], v[116:117], v[10:11] op_sel_hi:[0,1]
	v_pk_fma_f32 v[10:11], v[58:59], v[124:125], v[10:11] op_sel_hi:[1,0,1] neg_lo:[0,0,1] neg_hi:[0,0,1]
	v_mov_b32_e32 v58, v26
	v_pk_mul_f32 v[42:43], v[10:11], v[10:11]
	v_mov_b32_e32 v59, v128
	v_mov_b32_e32 v128, v27
	v_pk_add_f32 v[26:27], v[58:59], v[128:129]
	v_mov_b32_e32 v58, v42
	v_mov_b32_e32 v59, v126
	v_pk_add_f32 v[26:27], v[26:27], v[58:59]
	v_mov_b32_e32 v126, v43
	v_pk_add_f32 v[26:27], v[26:27], v[126:127]
	s_nop 1
	v_mov_b32_dpp v43, v27 quad_perm:[1,0,3,2] row_mask:0xf bank_mask:0xf
	v_mov_b32_dpp v42, v26 quad_perm:[1,0,3,2] row_mask:0xf bank_mask:0xf
	v_mov_b32_e32 v58, v44
	v_mov_b32_e32 v59, v60
	v_mov_b32_e32 v60, v45
	s_waitcnt lgkmcnt(0)
	v_pk_add_f32 v[26:27], v[26:27], v[42:43]
	s_nop 1
	v_mov_b32_dpp v43, v27 quad_perm:[2,3,0,1] row_mask:0xf bank_mask:0xf
	v_mov_b32_dpp v42, v26 quad_perm:[2,3,0,1] row_mask:0xf bank_mask:0xf
	s_waitcnt lgkmcnt(0)
	v_pk_add_f32 v[26:27], v[26:27], v[42:43]
	s_nop 1
	v_mov_b32_dpp v43, v27 row_half_mirror row_mask:0xf bank_mask:0xf
	v_mov_b32_dpp v42, v26 row_half_mirror row_mask:0xf bank_mask:0xf
	s_waitcnt lgkmcnt(0)
	v_pk_add_f32 v[26:27], v[26:27], v[42:43]
	s_nop 1
	v_mov_b32_dpp v43, v27 row_mirror row_mask:0xf bank_mask:0xf
	v_mov_b32_dpp v42, v26 row_mirror row_mask:0xf bank_mask:0xf
	s_waitcnt lgkmcnt(0)
	v_pk_add_f32 v[26:27], v[26:27], v[42:43]
	ds_bpermute_b32 v43, v1, v27
	ds_bpermute_b32 v42, v1, v26
	s_waitcnt lgkmcnt(0)
	v_pk_add_f32 v[26:27], v[26:27], v[42:43]
	s_nop 0
	v_pk_fma_f32 v[26:27], v[26:27], s[8:9], v[122:123] op_sel_hi:[1,0,0]
	v_mov_b32_e32 v43, v28
	v_mul_f32_e32 v42, 0x4b800000, v27
	v_cmp_gt_f32_e64 s[38:39], s66, v27
	v_cmp_gt_f32_e32 vcc, s66, v26
	v_mov_b32_e32 v28, v13
	v_cndmask_b32_e64 v27, v27, v42, s[38:39]
	v_rsq_f32_e32 v27, v27
	s_nop 0
	v_mul_f32_e32 v42, 0x45800000, v27
	v_cndmask_b32_e64 v27, v27, v42, s[38:39]
	v_mul_f32_e32 v126, v69, v27
	v_mul_f32_e32 v27, 0x4b800000, v26
	v_cndmask_b32_e32 v26, v26, v27, vcc
	v_rsq_f32_e32 v26, v26
	v_mov_b32_e32 v42, v12
	v_mul_f32_e32 v27, 0x45800000, v26
	v_cndmask_b32_e32 v26, v26, v27, vcc
	v_mul_f32_e32 v124, v69, v26
	ds_read2_b32 v[26:27], v71 offset1:32
	s_waitcnt lgkmcnt(0)
	v_pk_mul_f32 v[26:27], v[116:117], v[26:27] op_sel_hi:[0,1]
	v_pk_fma_f32 v[42:43], v[42:43], v[120:121], v[26:27] op_sel_hi:[1,0,1] neg_lo:[0,0,1] neg_hi:[0,0,1]
	ds_read2_b32 v[26:27], v71 offset0:64 offset1:96
	v_pk_mul_f32 v[128:129], v[42:43], v[42:43]
	s_waitcnt lgkmcnt(0)
	v_pk_mul_f32 v[26:27], v[116:117], v[26:27] op_sel_hi:[0,1]
	v_pk_fma_f32 v[26:27], v[58:59], v[120:121], v[26:27] op_sel_hi:[1,0,1] neg_lo:[0,0,1] neg_hi:[0,0,1]
	ds_read2_b32 v[58:59], v71 offset0:128 offset1:160
	v_pk_mul_f32 v[130:131], v[26:27], v[26:27]
	s_waitcnt lgkmcnt(0)
	v_pk_mul_f32 v[12:13], v[116:117], v[58:59] op_sel_hi:[0,1]
	v_pk_fma_f32 v[58:59], v[28:29], v[118:119], v[12:13] op_sel_hi:[1,0,1] neg_lo:[0,0,1] neg_hi:[0,0,1]
	ds_read2_b32 v[12:13], v71 offset0:192 offset1:224
	v_pk_mul_f32 v[28:29], v[58:59], v[58:59]
	v_add_u32_e32 v71, 0x3000, v67
	v_add_u32_e32 v67, 0x3400, v67
	s_waitcnt lgkmcnt(0)
	v_pk_mul_f32 v[12:13], v[116:117], v[12:13] op_sel_hi:[0,1]
	v_pk_fma_f32 v[12:13], v[60:61], v[118:119], v[12:13] op_sel_hi:[1,0,1] neg_lo:[0,0,1] neg_hi:[0,0,1]
	v_mov_b32_e32 v60, v28
	v_pk_mul_f32 v[44:45], v[12:13], v[12:13]
	v_mov_b32_e32 v61, v128
	v_mov_b32_e32 v128, v29
	v_pk_add_f32 v[28:29], v[60:61], v[128:129]
	v_mov_b32_e32 v60, v44
	v_mov_b32_e32 v61, v130
	v_pk_add_f32 v[28:29], v[28:29], v[60:61]
	v_mov_b32_e32 v130, v45
	v_pk_add_f32 v[28:29], v[28:29], v[130:131]
	s_nop 1
	v_mov_b32_dpp v45, v29 quad_perm:[1,0,3,2] row_mask:0xf bank_mask:0xf
	v_mov_b32_dpp v44, v28 quad_perm:[1,0,3,2] row_mask:0xf bank_mask:0xf
	v_mov_b32_e32 v60, v46
	v_mov_b32_e32 v61, v62
	v_mov_b32_e32 v62, v47
	s_waitcnt lgkmcnt(0)
	v_pk_add_f32 v[28:29], v[28:29], v[44:45]
	s_nop 1
	v_mov_b32_dpp v45, v29 quad_perm:[2,3,0,1] row_mask:0xf bank_mask:0xf
	v_mov_b32_dpp v44, v28 quad_perm:[2,3,0,1] row_mask:0xf bank_mask:0xf
	s_waitcnt lgkmcnt(0)
; __device__ __forceinline__ int crow(int r, int hi) { return (r & 3) + 8 * (r >> 2) + 4 * hi; }
; __device__ __forceinline__ void diff_unit(KP Pk, Frame& F, int l, int b, int h, int qrow0, int nkt) {
;     ...
;         float ssq[16];
; #pragma unroll
;         for (int r = 0; r < 16; ++r) { float a = 0.f;
; #pragma unroll
;             for (int nb = 0; nb < 4; ++nb) { const float v = O[nb][r] * rlr[r] - lam * ex[crow(r, hi) * 128 + nb * 32 + r32]; O[nb][r] = v; a += v * v; }
;             a += __shfl_xor(a, 1); a += __shfl_xor(a, 2); a += __shfl_xor(a, 4); a += __shfl_xor(a, 8); a += __shfl_xor(a, 16);
;             ssq[r] = rsqrtf(a * (1.f / 128.f) + NORM_EPS) * (1.f - lam_init); }
	v_pk_add_f32 v[28:29], v[28:29], v[44:45]
	s_nop 1
	v_mov_b32_dpp v45, v29 row_half_mirror row_mask:0xf bank_mask:0xf
	v_mov_b32_dpp v44, v28 row_half_mirror row_mask:0xf bank_mask:0xf
	s_waitcnt lgkmcnt(0)
	v_pk_add_f32 v[28:29], v[28:29], v[44:45]
	s_nop 1
	v_mov_b32_dpp v45, v29 row_mirror row_mask:0xf bank_mask:0xf
	v_mov_b32_dpp v44, v28 row_mirror row_mask:0xf bank_mask:0xf
	s_waitcnt lgkmcnt(0)
	v_pk_add_f32 v[28:29], v[28:29], v[44:45]
	ds_bpermute_b32 v45, v1, v29
	ds_bpermute_b32 v44, v1, v28
	s_waitcnt lgkmcnt(0)
	v_pk_add_f32 v[28:29], v[28:29], v[44:45]
	s_nop 0
	v_pk_fma_f32 v[28:29], v[28:29], s[8:9], v[122:123] op_sel_hi:[1,0,0]
	v_mov_b32_e32 v45, v30
	v_mul_f32_e32 v44, 0x4b800000, v29
	v_cmp_gt_f32_e64 s[38:39], s66, v29
	v_cmp_gt_f32_e32 vcc, s66, v28
	v_mov_b32_e32 v30, v15
	v_cndmask_b32_e64 v29, v29, v44, s[38:39]
	v_rsq_f32_e32 v29, v29
	s_nop 0
	v_mul_f32_e32 v44, 0x45800000, v29
	v_cndmask_b32_e64 v29, v29, v44, s[38:39]
	v_mul_f32_e32 v120, v69, v29
	v_mul_f32_e32 v29, 0x4b800000, v28
	v_cndmask_b32_e32 v28, v28, v29, vcc
	v_rsq_f32_e32 v28, v28
	v_mov_b32_e32 v44, v14
	v_mul_f32_e32 v29, 0x45800000, v28
	v_cndmask_b32_e32 v28, v28, v29, vcc
	v_mul_f32_e32 v118, v69, v28
	ds_read2_b32 v[28:29], v71 offset1:32
	s_waitcnt lgkmcnt(0)
	v_pk_mul_f32 v[28:29], v[116:117], v[28:29] op_sel_hi:[0,1]
	v_pk_fma_f32 v[44:45], v[44:45], v[114:115], v[28:29] op_sel_hi:[1,0,1] neg_lo:[0,0,1] neg_hi:[0,0,1]
	ds_read2_b32 v[28:29], v71 offset0:64 offset1:96
	v_pk_mul_f32 v[128:129], v[44:45], v[44:45]
	s_waitcnt lgkmcnt(0)
	v_pk_mul_f32 v[28:29], v[116:117], v[28:29] op_sel_hi:[0,1]
	v_pk_fma_f32 v[28:29], v[60:61], v[114:115], v[28:29] op_sel_hi:[1,0,1] neg_lo:[0,0,1] neg_hi:[0,0,1]
	ds_read2_b32 v[60:61], v71 offset0:128 offset1:160
	v_pk_mul_f32 v[130:131], v[28:29], v[28:29]
	s_waitcnt lgkmcnt(0)
	v_pk_mul_f32 v[14:15], v[116:117], v[60:61] op_sel_hi:[0,1]
	v_pk_fma_f32 v[60:61], v[30:31], v[112:113], v[14:15] op_sel_hi:[1,0,1] neg_lo:[0,0,1] neg_hi:[0,0,1]
	ds_read2_b32 v[14:15], v71 offset0:192 offset1:224
	v_pk_mul_f32 v[30:31], v[60:61], v[60:61]
	v_mov_b32_e32 v71, v0
	s_waitcnt lgkmcnt(0)
	v_pk_mul_f32 v[14:15], v[116:117], v[14:15] op_sel_hi:[0,1]
	v_pk_fma_f32 v[14:15], v[62:63], v[112:113], v[14:15] op_sel_hi:[1,0,1] neg_lo:[0,0,1] neg_hi:[0,0,1]
	v_mov_b32_e32 v62, v30
	v_pk_mul_f32 v[46:47], v[14:15], v[14:15]
	v_mov_b32_e32 v63, v128
	v_mov_b32_e32 v128, v31
	v_pk_add_f32 v[30:31], v[62:63], v[128:129]
	v_mov_b32_e32 v62, v46
	v_mov_b32_e32 v63, v130
	v_pk_add_f32 v[30:31], v[30:31], v[62:63]
	v_mov_b32_e32 v130, v47
	v_pk_add_f32 v[30:31], v[30:31], v[130:131]
	s_nop 1
	v_mov_b32_dpp v47, v31 quad_perm:[1,0,3,2] row_mask:0xf bank_mask:0xf
	v_mov_b32_dpp v46, v30 quad_perm:[1,0,3,2] row_mask:0xf bank_mask:0xf
	ds_read2_b32 v[130:131], v67 offset0:128 offset1:160
	v_mov_b32_e32 v128, v48
	v_mov_b32_e32 v129, v64
	v_mov_b32_e32 v64, v49
	s_waitcnt lgkmcnt(0)
	v_pk_add_f32 v[30:31], v[30:31], v[46:47]
	s_nop 1
	v_mov_b32_dpp v47, v31 quad_perm:[2,3,0,1] row_mask:0xf bank_mask:0xf
	v_mov_b32_dpp v46, v30 quad_perm:[2,3,0,1] row_mask:0xf bank_mask:0xf
	s_waitcnt lgkmcnt(0)
	v_pk_add_f32 v[30:31], v[30:31], v[46:47]
	s_nop 1
	v_mov_b32_dpp v47, v31 row_half_mirror row_mask:0xf bank_mask:0xf
	v_mov_b32_dpp v46, v30 row_half_mirror row_mask:0xf bank_mask:0xf
	s_waitcnt lgkmcnt(0)
	v_pk_add_f32 v[30:31], v[30:31], v[46:47]
	s_nop 1
	v_mov_b32_dpp v47, v31 row_mirror row_mask:0xf bank_mask:0xf
	v_mov_b32_dpp v46, v30 row_mirror row_mask:0xf bank_mask:0xf
	s_waitcnt lgkmcnt(0)
	v_pk_add_f32 v[30:31], v[30:31], v[46:47]
	ds_bpermute_b32 v47, v1, v31
	ds_bpermute_b32 v46, v1, v30
	s_waitcnt lgkmcnt(0)
	v_pk_add_f32 v[30:31], v[30:31], v[46:47]
	s_nop 0
	v_pk_fma_f32 v[30:31], v[30:31], s[8:9], v[122:123] op_sel_hi:[1,0,0]
	v_mov_b32_e32 v47, v32
	v_mul_f32_e32 v46, 0x4b800000, v31
	v_cmp_gt_f32_e64 s[38:39], s66, v31
	v_cmp_gt_f32_e32 vcc, s66, v30
	v_mov_b32_e32 v32, v17
	v_cndmask_b32_e64 v31, v31, v46, s[38:39]
	v_rsq_f32_e32 v31, v31
	s_nop 0
	v_mul_f32_e32 v46, 0x45800000, v31
	v_cndmask_b32_e64 v31, v31, v46, s[38:39]
	v_mul_f32_e32 v114, v69, v31
	v_mul_f32_e32 v31, 0x4b800000, v30
	v_cndmask_b32_e32 v30, v30, v31, vcc
	v_rsq_f32_e32 v30, v30
	v_mov_b32_e32 v46, v16
	v_pk_mul_f32 v[16:17], v[116:117], v[130:131] op_sel_hi:[0,1]
	v_pk_fma_f32 v[32:33], v[32:33], v[108:109], v[16:17] op_sel_hi:[1,0,1] neg_lo:[0,0,1] neg_hi:[0,0,1]
	v_mul_f32_e32 v31, 0x45800000, v30
	v_cndmask_b32_e32 v30, v30, v31, vcc
	v_mul_f32_e32 v112, v69, v30
	ds_read2_b32 v[30:31], v67 offset1:32
	ds_read2_b32 v[16:17], v67 offset0:192 offset1:224
	v_pk_mul_f32 v[130:131], v[32:33], v[32:33]
	s_waitcnt lgkmcnt(0)
	v_pk_mul_f32 v[30:31], v[116:117], v[30:31] op_sel_hi:[0,1]
	v_pk_fma_f32 v[46:47], v[46:47], v[110:111], v[30:31] op_sel_hi:[1,0,1] neg_lo:[0,0,1] neg_hi:[0,0,1]
	ds_read2_b32 v[30:31], v67 offset0:64 offset1:96
	s_waitcnt lgkmcnt(0)
	v_pk_mul_f32 v[16:17], v[116:117], v[16:17] op_sel_hi:[0,1]
	v_pk_mul_f32 v[62:63], v[46:47], v[46:47]
	v_pk_fma_f32 v[16:17], v[64:65], v[108:109], v[16:17] op_sel_hi:[1,0,1] neg_lo:[0,0,1] neg_hi:[0,0,1]
	v_mov_b32_e32 v64, v130
	s_waitcnt lgkmcnt(0)
	v_pk_mul_f32 v[30:31], v[116:117], v[30:31] op_sel_hi:[0,1]
	v_pk_fma_f32 v[30:31], v[128:129], v[110:111], v[30:31] op_sel_hi:[1,0,1] neg_lo:[0,0,1] neg_hi:[0,0,1]
	v_pk_mul_f32 v[48:49], v[16:17], v[16:17]
	v_pk_mul_f32 v[128:129], v[30:31], v[30:31]
	v_mov_b32_e32 v65, v62
	v_mov_b32_e32 v62, v131
	v_pk_add_f32 v[62:63], v[64:65], v[62:63]
	v_mov_b32_e32 v64, v48
	v_mov_b32_e32 v65, v128
	v_pk_add_f32 v[62:63], v[62:63], v[64:65]
	v_mov_b32_e32 v128, v49
	v_pk_add_f32 v[48:49], v[62:63], v[128:129]
	s_nop 1
	v_mov_b32_dpp v63, v49 quad_perm:[1,0,3,2] row_mask:0xf bank_mask:0xf
	v_mov_b32_dpp v62, v48 quad_perm:[1,0,3,2] row_mask:0xf bank_mask:0xf
	v_mov_b32_e32 v65, v0
	s_waitcnt lgkmcnt(0)
; __device__ __forceinline__ unsigned f2bf(float f) { unsigned u = __builtin_bit_cast(unsigned, f); return (u + 0x7fffu + ((u >> 16) & 1u)) >> 16; }
; __device__ __forceinline__ unsigned char f8_1(float a) { a = fminf(fmaxf(a, -448.f), 448.f); return (unsigned char)(__builtin_amdgcn_cvt_pk_fp8_f32(a, a, 0, false) & 0xff); }
; __device__ __forceinline__ int crow(int r, int hi) { return (r & 3) + 8 * (r >> 2) + 4 * hi; }
; __device__ __forceinline__ void diff_unit(KP Pk, Frame& F, int l, int b, int h, int qrow0, int nkt) {
;     ...
;         for (int r = 0; r < 16; ++r) { float a = 0.f;
; #pragma unroll
;             for (int nb = 0; nb < 4; ++nb) { const float v = O[nb][r] * rlr[r] - lam * ex[crow(r, hi) * 128 + nb * 32 + r32]; O[nb][r] = v; a += v * v; }
;             a += __shfl_xor(a, 1); a += __shfl_xor(a, 2); a += __shfl_xor(a, 4); a += __shfl_xor(a, 8); a += __shfl_xor(a, 16);
;             ssq[r] = rsqrtf(a * (1.f / 128.f) + NORM_EPS) * (1.f - lam_init); }
;         unsigned char* mix = ws + WS_H + ((size_t)(qrow0 + 32 * rb) * D + 1536 + h * 128) * MIXB;
; #pragma unroll
;         for (int nb = 0; nb < 4; ++nb) { const float w = Pk->in[I_DSUB][l * 128 + nb * 32 + r32];
; #pragma unroll
;             for (int r = 0; r < 16; ++r) { const float y = O[nb][r] * ssq[r] * w; const size_t e = (size_t)crow(r, hi) * D + nb * 32 + r32; if (WOUT_F8) mix[e] = f8_1(y); else ((bf16_t*)mix)[e] = (bf16_t)f2bf(y); } }
	v_pk_add_f32 v[48:49], v[48:49], v[62:63]
	s_nop 1
	v_mov_b32_dpp v63, v49 quad_perm:[2,3,0,1] row_mask:0xf bank_mask:0xf
	v_mov_b32_dpp v62, v48 quad_perm:[2,3,0,1] row_mask:0xf bank_mask:0xf
	s_waitcnt lgkmcnt(0)
	v_pk_add_f32 v[48:49], v[48:49], v[62:63]
	s_nop 1
	v_mov_b32_dpp v63, v49 row_half_mirror row_mask:0xf bank_mask:0xf
	v_mov_b32_dpp v62, v48 row_half_mirror row_mask:0xf bank_mask:0xf
	s_waitcnt lgkmcnt(0)
	v_pk_add_f32 v[48:49], v[48:49], v[62:63]
	s_nop 1
	v_mov_b32_dpp v63, v49 row_mirror row_mask:0xf bank_mask:0xf
	v_mov_b32_dpp v62, v48 row_mirror row_mask:0xf bank_mask:0xf
	s_waitcnt lgkmcnt(0)
	v_pk_add_f32 v[48:49], v[48:49], v[62:63]
	ds_bpermute_b32 v63, v1, v49
	ds_bpermute_b32 v62, v1, v48
	s_waitcnt lgkmcnt(0)
	v_pk_add_f32 v[48:49], v[48:49], v[62:63]
	s_nop 0
	v_pk_fma_f32 v[48:49], v[48:49], s[8:9], v[122:123] op_sel_hi:[1,0,0]
	v_mul_f32_e32 v62, v100, v111
	v_mul_f32_e32 v1, 0x4b800000, v49
	v_cmp_gt_f32_e64 s[38:39], s66, v49
	v_cmp_gt_f32_e32 vcc, s66, v48
	s_lshl_b64 s[8:9], s[40:41], 11
	v_cndmask_b32_e64 v1, v49, v1, s[38:39]
	v_rsq_f32_e32 v1, v1
	s_add_u32 s5, s5, s8
	v_readlane_b32 s8, v254, 62
	s_addc_u32 s9, s8, s9
	v_mul_f32_e32 v49, 0x45800000, v1
	v_cndmask_b32_e64 v1, v1, v49, s[38:39]
	v_mul_f32_e32 v108, v69, v1
	v_mul_f32_e32 v1, 0x4b800000, v48
	v_cndmask_b32_e32 v1, v48, v1, vcc
	v_rsq_f32_e32 v1, v1
	s_add_u32 s8, s5, s18
	s_addc_u32 s9, s9, 0
	v_mul_f32_e32 v48, 0x45800000, v1
	v_cndmask_b32_e32 v1, v1, v48, vcc
	v_lshl_or_b32 v48, s4, 7, v104
	v_ashrrev_i32_e32 v49, 31, v48
	v_lshl_add_u64 v[48:49], v[48:49], 2, v[106:107]
	global_load_dword v67, v[48:49], off
	global_load_dword v236, v[48:49], off offset:128
	global_load_dword v250, v[48:49], off offset:256
	global_load_dword v251, v[48:49], off offset:384
	v_mul_f32_e32 v1, v69, v1
	v_lshl_add_u64 v[104:105], s[8:9], 0, v[104:105]
	v_lshl_add_u64 v[92:93], v[104:105], 0, v[92:93]
	v_lshl_add_u64 v[90:91], v[104:105], 0, v[90:91]
	v_lshl_add_u64 v[88:89], v[104:105], 0, v[88:89]
	v_lshl_add_u64 v[86:87], v[104:105], 0, v[86:87]
	v_lshl_add_u64 v[84:85], v[104:105], 0, v[84:85]
	v_lshl_add_u64 v[82:83], v[104:105], 0, v[82:83]
	v_lshl_add_u64 v[80:81], v[104:105], 0, v[80:81]
	v_lshl_add_u64 v[78:79], v[104:105], 0, v[78:79]
	v_lshl_add_u64 v[74:75], v[104:105], 0, v[74:75]
	v_lshl_add_u64 v[72:73], v[104:105], 0, v[72:73]
	v_lshl_add_u64 v[94:95], v[104:105], 0, v[94:95]
	s_waitcnt vmcnt(0)
	v_mul_f32_e32 v64, v62, v67
	v_med3_f32 v64, v64, s83, v238
	v_cvt_pk_fp8_f32 v65, v64, v64
	v_mul_f32_e32 v64, v102, v109
	v_mul_f32_e32 v69, v64, v67
	v_med3_f32 v69, v69, s83, v238
	v_mul_f32_e32 v34, v34, v67
	v_cvt_pk_fp8_f32 v71, v69, v69
	v_med3_f32 v34, v34, s83, v238
	v_mov_b32_e32 v69, v0
	v_mul_f32_e32 v20, v20, v67
	v_cvt_pk_fp8_f32 v69, v34, v34
	v_med3_f32 v20, v20, s83, v238
	v_mov_b32_e32 v34, v0
	v_cvt_pk_fp8_f32 v34, v20, v20
	v_mul_f32_e32 v20, v36, v119
	v_mul_f32_e32 v20, v20, v67
	v_med3_f32 v20, v20, s83, v238
	global_store_byte v[92:93], v34, off
	v_mov_b32_e32 v34, v0
	v_cvt_pk_fp8_f32 v34, v20, v20
	v_mul_f32_e32 v20, v52, v117
	v_mul_f32_e32 v20, v20, v67
	v_med3_f32 v20, v20, s83, v238
	global_store_byte v[90:91], v34, off
	v_mov_b32_e32 v34, v0
	v_cvt_pk_fp8_f32 v34, v20, v20
	v_mul_f32_e32 v20, v38, v125
	v_mul_f32_e32 v20, v20, v67
	v_med3_f32 v20, v20, s83, v238
	global_store_byte v[88:89], v34, off
	v_mov_b32_e32 v34, v0
	v_cvt_pk_fp8_f32 v34, v20, v20
	v_mul_f32_e32 v20, v54, v121
	v_mul_f32_e32 v20, v20, v67
	v_med3_f32 v20, v20, s83, v238
	global_store_byte v[86:87], v34, off
	v_mov_b32_e32 v34, v0
	v_cvt_pk_fp8_f32 v34, v20, v20
	v_mul_f32_e32 v20, v40, v126
	v_mul_f32_e32 v20, v20, v67
	v_med3_f32 v20, v20, s83, v238
	global_store_byte v[84:85], v34, off
	v_mov_b32_e32 v34, v0
	v_cvt_pk_fp8_f32 v34, v20, v20
	v_mul_f32_e32 v20, v56, v124
	v_mul_f32_e32 v20, v20, v67
	v_med3_f32 v20, v20, s83, v238
	global_store_byte v[82:83], v34, off
	v_mov_b32_e32 v34, v0
	v_cvt_pk_fp8_f32 v34, v20, v20
	v_mul_f32_e32 v20, v42, v120
	v_mul_f32_e32 v20, v20, v67
	v_med3_f32 v20, v20, s83, v238
	global_store_byte v[80:81], v34, off
	v_mov_b32_e32 v34, v0
	v_cvt_pk_fp8_f32 v34, v20, v20
	v_mul_f32_e32 v20, v58, v118
	v_mul_f32_e32 v20, v20, v67
	v_med3_f32 v20, v20, s83, v238
	global_store_byte v[78:79], v34, off
	v_mov_b32_e32 v34, v0
	v_cvt_pk_fp8_f32 v34, v20, v20
	v_mul_f32_e32 v20, v44, v114
	v_mul_f32_e32 v20, v20, v67
	v_med3_f32 v20, v20, s83, v238
	global_store_byte v[74:75], v34, off
	v_mov_b32_e32 v34, v0
	v_cvt_pk_fp8_f32 v34, v20, v20
	v_lshlrev_b64 v[62:63], 11, v[98:99]
	v_mul_f32_e32 v20, v60, v112
	v_lshl_add_u64 v[62:63], v[104:105], 0, v[62:63]
	v_mul_f32_e32 v20, v20, v67
	global_store_byte v[62:63], v65, off
	v_lshlrev_b64 v[64:65], 11, v[96:97]
	global_store_byte v[72:73], v34, off
	v_med3_f32 v20, v20, s83, v238
	v_mov_b32_e32 v34, v0
	v_lshl_add_u64 v[64:65], v[104:105], 0, v[64:65]
	v_cvt_pk_fp8_f32 v34, v20, v20
	global_store_byte v[64:65], v71, off
	v_ashrrev_i32_e32 v71, 31, v70
	v_lshlrev_b64 v[70:71], 11, v[70:71]
	v_mul_f32_e32 v20, v46, v108
	v_lshl_add_u64 v[70:71], v[104:105], 0, v[70:71]
	v_mul_f32_e32 v20, v67, v20
	global_store_byte v[70:71], v34, off
	v_med3_f32 v20, v20, s83, v238
	v_mov_b32_e32 v34, v0
	v_cvt_pk_fp8_f32 v34, v20, v20
	v_mul_f32_e32 v20, v32, v1
	v_mul_f32_e32 v20, v67, v20
	v_med3_f32 v20, v20, s83, v238
	v_mov_b32_e32 v32, v0
	v_cvt_pk_fp8_f32 v32, v20, v20
	global_store_byte v[94:95], v69, off
	v_ashrrev_i32_e32 v69, 31, v68
	v_ashrrev_i32_e32 v67, 31, v66
	v_lshlrev_b64 v[68:69], 11, v[68:69]
	v_lshlrev_b64 v[66:67], 11, v[66:67]
	v_lshl_add_u64 v[68:69], v[104:105], 0, v[68:69]
; __device__ __forceinline__ unsigned f2bf(float f) { unsigned u = __builtin_bit_cast(unsigned, f); return (u + 0x7fffu + ((u >> 16) & 1u)) >> 16; }
; __device__ __forceinline__ unsigned char f8_1(float a) { a = fminf(fmaxf(a, -448.f), 448.f); return (unsigned char)(__builtin_amdgcn_cvt_pk_fp8_f32(a, a, 0, false) & 0xff); }
; __device__ __forceinline__ int crow(int r, int hi) { return (r & 3) + 8 * (r >> 2) + 4 * hi; }
; __device__ __forceinline__ void diff_unit(KP Pk, Frame& F, int l, int b, int h, int qrow0, int nkt) {
;     ...
; #pragma unroll
;         for (int nb = 0; nb < 4; ++nb) { const float w = Pk->in[I_DSUB][l * 128 + nb * 32 + r32];
; #pragma unroll
;             for (int r = 0; r < 16; ++r) { const float y = O[nb][r] * ssq[r] * w; const size_t e = (size_t)crow(r, hi) * D + nb * 32 + r32; if (WOUT_F8) mix[e] = f8_1(y); else ((bf16_t*)mix)[e] = (bf16_t)f2bf(y); } }
	v_lshl_add_u64 v[66:67], v[104:105], 0, v[66:67]
	global_store_byte v[68:69], v34, off
	global_store_byte v[66:67], v32, off
	v_mov_b32_e32 v20, v236
	v_mul_f32_e32 v32, v101, v111
	v_mov_b32_e32 v34, v0
	v_mul_f32_e32 v32, v32, v20
	v_med3_f32 v32, v32, s83, v238
	v_cvt_pk_fp8_f32 v34, v32, v32
	v_mul_f32_e32 v32, v103, v109
	v_mul_f32_e32 v32, v32, v20
	v_med3_f32 v32, v32, s83, v238
	global_store_byte v[62:63], v34, off offset:32
	v_mov_b32_e32 v34, v0
	v_cvt_pk_fp8_f32 v34, v32, v32
	v_mul_f32_e32 v32, v35, v115
	v_mul_f32_e32 v32, v32, v20
	v_med3_f32 v32, v32, s83, v238
	global_store_byte v[64:65], v34, off offset:32
	v_mov_b32_e32 v34, v0
	v_mul_f32_e32 v21, v21, v20
	v_cvt_pk_fp8_f32 v34, v32, v32
	v_med3_f32 v21, v21, s83, v238
	v_mov_b32_e32 v32, v0
	v_cvt_pk_fp8_f32 v32, v21, v21
	v_mul_f32_e32 v21, v37, v119
	v_mul_f32_e32 v21, v21, v20
	v_med3_f32 v21, v21, s83, v238
	global_store_byte v[92:93], v32, off offset:32
	v_mov_b32_e32 v32, v0
	v_cvt_pk_fp8_f32 v32, v21, v21
	v_mul_f32_e32 v21, v53, v117
	v_mul_f32_e32 v21, v21, v20
	v_med3_f32 v21, v21, s83, v238
	global_store_byte v[90:91], v32, off offset:32
	v_mov_b32_e32 v32, v0
	v_cvt_pk_fp8_f32 v32, v21, v21
	v_mul_f32_e32 v21, v39, v125
	v_mul_f32_e32 v21, v21, v20
	v_med3_f32 v21, v21, s83, v238
	global_store_byte v[88:89], v32, off offset:32
	v_mov_b32_e32 v32, v0
	v_cvt_pk_fp8_f32 v32, v21, v21
	v_mul_f32_e32 v21, v55, v121
	v_mul_f32_e32 v21, v21, v20
	v_med3_f32 v21, v21, s83, v238
	global_store_byte v[86:87], v32, off offset:32
	v_mov_b32_e32 v32, v0
	v_cvt_pk_fp8_f32 v32, v21, v21
	v_mul_f32_e32 v21, v41, v126
	v_mul_f32_e32 v21, v21, v20
	v_med3_f32 v21, v21, s83, v238
	global_store_byte v[84:85], v32, off offset:32
	v_mov_b32_e32 v32, v0
	v_cvt_pk_fp8_f32 v32, v21, v21
	v_mul_f32_e32 v21, v57, v124
	v_mul_f32_e32 v21, v21, v20
	v_med3_f32 v21, v21, s83, v238
	global_store_byte v[82:83], v32, off offset:32
	v_mov_b32_e32 v32, v0
	v_cvt_pk_fp8_f32 v32, v21, v21
	v_mul_f32_e32 v21, v43, v120
	v_mul_f32_e32 v21, v21, v20
	v_med3_f32 v21, v21, s83, v238
	global_store_byte v[80:81], v32, off offset:32
	v_mov_b32_e32 v32, v0
	v_cvt_pk_fp8_f32 v32, v21, v21
	v_mul_f32_e32 v21, v59, v118
	v_mul_f32_e32 v21, v21, v20
	v_med3_f32 v21, v21, s83, v238
	global_store_byte v[78:79], v32, off offset:32
	v_mov_b32_e32 v32, v0
	v_cvt_pk_fp8_f32 v32, v21, v21
	v_mul_f32_e32 v21, v45, v114
	v_mul_f32_e32 v21, v21, v20
	v_med3_f32 v21, v21, s83, v238
	global_store_byte v[74:75], v32, off offset:32
	v_mov_b32_e32 v32, v0
	v_cvt_pk_fp8_f32 v32, v21, v21
	v_mul_f32_e32 v21, v61, v112
	v_mul_f32_e32 v21, v21, v20
	v_med3_f32 v21, v21, s83, v238
	global_store_byte v[72:73], v32, off offset:32
	v_mov_b32_e32 v32, v0
	v_cvt_pk_fp8_f32 v32, v21, v21
	v_mul_f32_e32 v21, v47, v108
	v_mul_f32_e32 v21, v21, v20
	v_med3_f32 v21, v21, s83, v238
	global_store_byte v[70:71], v32, off offset:32
	v_mov_b32_e32 v32, v0
	v_cvt_pk_fp8_f32 v32, v21, v21
	v_mul_f32_e32 v21, v33, v1
	v_mul_f32_e32 v20, v21, v20
	v_med3_f32 v20, v20, s83, v238
	v_mov_b32_e32 v21, v0
	v_cvt_pk_fp8_f32 v21, v20, v20
	global_store_byte v[94:95], v34, off offset:32
	global_store_byte v[68:69], v32, off offset:32
	v_mov_b32_e32 v32, v0
	global_store_byte v[66:67], v21, off offset:32
	v_mov_b32_e32 v20, v250
	v_mul_f32_e32 v21, v77, v111
	v_mul_f32_e32 v21, v21, v20
	v_med3_f32 v21, v21, s83, v238
	v_mul_f32_e32 v2, v2, v20
	v_cvt_pk_fp8_f32 v32, v21, v21
	v_med3_f32 v2, v2, s83, v238
	v_mov_b32_e32 v21, v0
	v_cvt_pk_fp8_f32 v21, v2, v2
	v_mul_f32_e32 v2, v18, v115
	v_mul_f32_e32 v2, v2, v20
	v_med3_f32 v2, v2, s83, v238
	v_mov_b32_e32 v18, v0
	v_cvt_pk_fp8_f32 v18, v2, v2
	v_mul_f32_e32 v2, v4, v113
	v_mul_f32_e32 v2, v2, v20
	v_med3_f32 v2, v2, s83, v238
	v_mov_b32_e32 v4, v0
	v_cvt_pk_fp8_f32 v4, v2, v2
	v_mul_f32_e32 v2, v50, v119
	v_mul_f32_e32 v2, v2, v20
	v_med3_f32 v2, v2, s83, v238
	global_store_byte v[92:93], v4, off offset:64
	v_mov_b32_e32 v4, v0
	v_cvt_pk_fp8_f32 v4, v2, v2
	v_mul_f32_e32 v2, v6, v117
	v_mul_f32_e32 v2, v2, v20
	v_med3_f32 v2, v2, s83, v238
	global_store_byte v[90:91], v4, off offset:64
	v_mov_b32_e32 v4, v0
	v_cvt_pk_fp8_f32 v4, v2, v2
	v_mul_f32_e32 v2, v22, v125
	v_mul_f32_e32 v2, v2, v20
	v_med3_f32 v2, v2, s83, v238
	global_store_byte v[88:89], v4, off offset:64
	v_mov_b32_e32 v4, v0
	v_cvt_pk_fp8_f32 v4, v2, v2
	v_mul_f32_e32 v2, v8, v121
	v_mul_f32_e32 v2, v2, v20
	v_med3_f32 v2, v2, s83, v238
	global_store_byte v[86:87], v4, off offset:64
	v_mov_b32_e32 v4, v0
	v_cvt_pk_fp8_f32 v4, v2, v2
	v_mul_f32_e32 v2, v24, v126
; __device__ __forceinline__ unsigned f2bf(float f) { unsigned u = __builtin_bit_cast(unsigned, f); return (u + 0x7fffu + ((u >> 16) & 1u)) >> 16; }
; __device__ __forceinline__ unsigned char f8_1(float a) { a = fminf(fmaxf(a, -448.f), 448.f); return (unsigned char)(__builtin_amdgcn_cvt_pk_fp8_f32(a, a, 0, false) & 0xff); }
; __device__ __forceinline__ int crow(int r, int hi) { return (r & 3) + 8 * (r >> 2) + 4 * hi; }
; __device__ __forceinline__ void diff_unit(KP Pk, Frame& F, int l, int b, int h, int qrow0, int nkt) {
;     ...
; #pragma unroll
;         for (int nb = 0; nb < 4; ++nb) { const float w = Pk->in[I_DSUB][l * 128 + nb * 32 + r32];
; #pragma unroll
;             for (int r = 0; r < 16; ++r) { const float y = O[nb][r] * ssq[r] * w; const size_t e = (size_t)crow(r, hi) * D + nb * 32 + r32; if (WOUT_F8) mix[e] = f8_1(y); else ((bf16_t*)mix)[e] = (bf16_t)f2bf(y); } }
	v_mul_f32_e32 v2, v2, v20
	v_med3_f32 v2, v2, s83, v238
	global_store_byte v[84:85], v4, off offset:64
	v_mov_b32_e32 v4, v0
	v_cvt_pk_fp8_f32 v4, v2, v2
	v_mul_f32_e32 v2, v10, v124
	v_mul_f32_e32 v2, v2, v20
	v_med3_f32 v2, v2, s83, v238
	global_store_byte v[82:83], v4, off offset:64
	v_mov_b32_e32 v4, v0
	v_cvt_pk_fp8_f32 v4, v2, v2
	v_mul_f32_e32 v2, v26, v120
	v_mul_f32_e32 v2, v2, v20
	v_med3_f32 v2, v2, s83, v238
	global_store_byte v[80:81], v4, off offset:64
	v_mov_b32_e32 v4, v0
	v_cvt_pk_fp8_f32 v4, v2, v2
	v_mul_f32_e32 v2, v12, v118
	v_mul_f32_e32 v2, v2, v20
	v_med3_f32 v2, v2, s83, v238
	global_store_byte v[78:79], v4, off offset:64
	v_mov_b32_e32 v4, v0
	v_cvt_pk_fp8_f32 v4, v2, v2
	v_mul_f32_e32 v2, v28, v114
	v_mul_f32_e32 v2, v2, v20
	v_med3_f32 v2, v2, s83, v238
	global_store_byte v[74:75], v4, off offset:64
	v_mov_b32_e32 v4, v0
	v_cvt_pk_fp8_f32 v4, v2, v2
	v_mul_f32_e32 v2, v14, v112
	v_mul_f32_e32 v2, v2, v20
	v_med3_f32 v2, v2, s83, v238
	global_store_byte v[72:73], v4, off offset:64
	v_mov_b32_e32 v4, v0
	v_cvt_pk_fp8_f32 v4, v2, v2
	v_mul_f32_e32 v2, v30, v108
	v_mul_f32_e32 v2, v2, v20
	v_med3_f32 v2, v2, s83, v238
	global_store_byte v[70:71], v4, off offset:64
	v_mov_b32_e32 v4, v0
	v_cvt_pk_fp8_f32 v4, v2, v2
	v_mul_f32_e32 v2, v16, v1
	v_mul_f32_e32 v2, v2, v20
	v_med3_f32 v2, v2, s83, v238
	global_store_byte v[68:69], v4, off offset:64
	v_mov_b32_e32 v4, v0
	v_cvt_pk_fp8_f32 v4, v2, v2
	global_store_byte v[62:63], v32, off offset:64
	global_store_byte v[64:65], v21, off offset:64
	global_store_byte v[94:95], v18, off offset:64
	global_store_byte v[66:67], v4, off offset:64
	v_mov_b32_e32 v2, v251
	v_mul_f32_e32 v4, v76, v111
	v_mov_b32_e32 v6, v0
	v_mul_f32_e32 v1, v17, v1
	v_mul_f32_e32 v4, v4, v2
	v_med3_f32 v4, v4, s83, v238
	v_mul_f32_e32 v3, v3, v2
	v_cvt_pk_fp8_f32 v6, v4, v4
	v_med3_f32 v3, v3, s83, v238
	v_mov_b32_e32 v4, v0
	v_cvt_pk_fp8_f32 v4, v3, v3
	v_mul_f32_e32 v3, v19, v115
	v_mul_f32_e32 v3, v3, v2
	v_med3_f32 v3, v3, s83, v238
	global_store_byte v[64:65], v4, off offset:96
	v_mov_b32_e32 v4, v0
	v_cvt_pk_fp8_f32 v4, v3, v3
	v_mul_f32_e32 v3, v5, v113
	v_mul_f32_e32 v3, v3, v2
	v_med3_f32 v3, v3, s83, v238
	global_store_byte v[94:95], v4, off offset:96
	v_mov_b32_e32 v4, v0
	v_cvt_pk_fp8_f32 v4, v3, v3
	v_mul_f32_e32 v3, v51, v119
	v_mul_f32_e32 v3, v3, v2
	v_med3_f32 v3, v3, s83, v238
	global_store_byte v[92:93], v4, off offset:96
	v_mov_b32_e32 v4, v0
	v_cvt_pk_fp8_f32 v4, v3, v3
	v_mul_f32_e32 v3, v7, v117
	v_mul_f32_e32 v3, v3, v2
	v_med3_f32 v3, v3, s83, v238
	global_store_byte v[90:91], v4, off offset:96
	v_mov_b32_e32 v4, v0
	v_cvt_pk_fp8_f32 v4, v3, v3
	v_mul_f32_e32 v3, v23, v125
	v_mul_f32_e32 v3, v3, v2
	v_med3_f32 v3, v3, s83, v238
	global_store_byte v[88:89], v4, off offset:96
	v_mov_b32_e32 v4, v0
	v_cvt_pk_fp8_f32 v4, v3, v3
	v_mul_f32_e32 v3, v9, v121
	v_mul_f32_e32 v3, v3, v2
	v_med3_f32 v3, v3, s83, v238
	global_store_byte v[86:87], v4, off offset:96
	v_mov_b32_e32 v4, v0
	v_cvt_pk_fp8_f32 v4, v3, v3
	v_mul_f32_e32 v3, v25, v126
	v_mul_f32_e32 v3, v3, v2
	v_med3_f32 v3, v3, s83, v238
	global_store_byte v[84:85], v4, off offset:96
	v_mov_b32_e32 v4, v0
	v_cvt_pk_fp8_f32 v4, v3, v3
	v_mul_f32_e32 v3, v11, v124
	v_mul_f32_e32 v3, v3, v2
	v_med3_f32 v3, v3, s83, v238
	global_store_byte v[82:83], v4, off offset:96
	v_mov_b32_e32 v4, v0
	v_cvt_pk_fp8_f32 v4, v3, v3
	v_mul_f32_e32 v3, v27, v120
	v_mul_f32_e32 v3, v3, v2
	v_med3_f32 v3, v3, s83, v238
	global_store_byte v[80:81], v4, off offset:96
	v_mov_b32_e32 v4, v0
	v_cvt_pk_fp8_f32 v4, v3, v3
	v_mul_f32_e32 v3, v13, v118
	v_mul_f32_e32 v3, v3, v2
	v_med3_f32 v3, v3, s83, v238
	global_store_byte v[78:79], v4, off offset:96
	v_mov_b32_e32 v4, v0
	v_cvt_pk_fp8_f32 v4, v3, v3
	v_mul_f32_e32 v3, v29, v114
	v_mul_f32_e32 v3, v3, v2
	v_med3_f32 v3, v3, s83, v238
	global_store_byte v[74:75], v4, off offset:96
	v_mov_b32_e32 v4, v0
	v_cvt_pk_fp8_f32 v4, v3, v3
	v_mul_f32_e32 v3, v15, v112
	v_mul_f32_e32 v3, v3, v2
	v_med3_f32 v3, v3, s83, v238
	global_store_byte v[72:73], v4, off offset:96
	v_mov_b32_e32 v4, v0
	v_cvt_pk_fp8_f32 v4, v3, v3
	v_mul_f32_e32 v3, v31, v108
	v_mul_f32_e32 v3, v3, v2
	v_mul_f32_e32 v1, v1, v2
	global_store_byte v[70:71], v4, off offset:96
	v_med3_f32 v3, v3, s83, v238
	v_mov_b32_e32 v4, v0
	v_med3_f32 v1, v1, s83, v238
	v_mov_b32_e32 v2, v0
	v_cvt_pk_fp8_f32 v4, v3, v3
	v_cvt_pk_fp8_f32 v2, v1, v1
	global_store_byte v[62:63], v6, off offset:96
	global_store_byte v[68:69], v4, off offset:96
	global_store_byte v[66:67], v2, off offset:96

; __device__ __forceinline__ int crow(int r, int hi) { return (r & 3) + 8 * (r >> 2) + 4 * hi; }
; __device__ __forceinline__ float wave_sum(float v) {
; #pragma unroll
;     for (int o = 1; o < 64; o <<= 1) v += __shfl_xor(v, o);
;     return v;
; __device__ __forceinline__ void diff_unit(KP Pk, Frame& F, int l, int b, int h, int qrow0, int nkt) {
;     ...
;     if (m == 0) {
;         const float* dl = Pk->in[I_DLAM] + l * 256; const float lam_init = __builtin_bit_cast(float, __builtin_amdgcn_readfirstlane(__builtin_bit_cast(int, l == 0 ? 0.2f : (0.8f - 0.6f * 0.74081822068f))));
;         const float lam = expf(wave_sum(dl[ln_] * dl[64 + ln_])) - expf(wave_sum(dl[128 + ln_] * dl[192 + ln_])) + lam_init;
;         float ssq[16];
; #pragma unroll
;         for (int r = 0; r < 16; ++r) { float a = 0.f;
; #pragma unroll
;             for (int nb = 0; nb < 4; ++nb) { const float v = O[nb][r] * rlr[r] - lam * ex[crow(r, hi) * 128 + nb * 32 + r32]; O[nb][r] = v; a += v * v; }
;             a += __shfl_xor(a, 1); a += __shfl_xor(a, 2); a += __shfl_xor(a, 4); a += __shfl_xor(a, 8); a += __shfl_xor(a, 16);
;             ssq[r] = rsqrtf(a * (1.f / 128.f) + NORM_EPS) * (1.f - lam_init); }
.LBB0_637:
	v_readlane_b32 s26, v253, 17
	v_readlane_b32 s27, v253, 18
	s_andn2_b64 vcc, exec, s[26:27]
	s_waitcnt lgkmcnt(0)
	s_barrier
	s_cbranch_vccnz .LBB0_639
	s_load_dwordx4 s[44:47], s[8:9], 0xd8
	s_lshl_b32 s8, s4, 8
	s_ashr_i32 s9, s8, 31
	s_lshl_b64 s[8:9], s[8:9], 2
	v_ashrrev_i32_e32 v101, 31, v100
	s_waitcnt lgkmcnt(0)
	s_add_u32 s8, s44, s8
	s_addc_u32 s9, s45, s9
	v_lshl_add_u64 v[100:101], v[100:101], 2, s[8:9]
	global_load_dword v69, v[100:101], off
	global_load_dword v71, v[100:101], off offset:256
	global_load_dword v250, v[100:101], off offset:512
	global_load_dword v251, v[100:101], off offset:768
	s_cmp_eq_u32 s4, 0
	s_mov_b32 s5, 0x3e4ccccd
	s_cselect_b32 s5, s5, 0x3eb60549
	v_mov_b32_e32 v102, v2
	v_mov_b32_e32 v103, v18
	v_mov_b32_e32 v146, v50
	v_mov_b32_e32 v147, v34
	v_mov_b32_e32 v18, v3
	v_mov_b32_e32 v50, v35
	s_mov_b32 s8, 0x358637bd
	v_mov_b32_e32 v106, s46
	v_mov_b32_e32 v107, s47
	s_ashr_i32 s41, s40, 31
	v_mov_b32_e32 v105, v0
	v_ashrrev_i32_e32 v93, 31, v92
	v_lshlrev_b64 v[92:93], 11, v[92:93]
	v_ashrrev_i32_e32 v91, 31, v90
	v_lshlrev_b64 v[90:91], 11, v[90:91]
	v_ashrrev_i32_e32 v89, 31, v88
	v_lshlrev_b64 v[88:89], 11, v[88:89]
	v_ashrrev_i32_e32 v87, 31, v86
	v_lshlrev_b64 v[86:87], 11, v[86:87]
	v_ashrrev_i32_e32 v85, 31, v84
	v_lshlrev_b64 v[84:85], 11, v[84:85]
	v_ashrrev_i32_e32 v83, 31, v82
	v_lshlrev_b64 v[82:83], 11, v[82:83]
	v_ashrrev_i32_e32 v81, 31, v80
	v_lshlrev_b64 v[80:81], 11, v[80:81]
	v_ashrrev_i32_e32 v79, 31, v78
	v_lshlrev_b64 v[78:79], 11, v[78:79]
	v_ashrrev_i32_e32 v99, 31, v98
	v_ashrrev_i32_e32 v97, 31, v96
	v_ashrrev_i32_e32 v95, 31, v94
	v_lshlrev_b64 v[94:95], 11, v[94:95]
	s_waitcnt vmcnt(0)
	v_mul_f32_e32 v73, v69, v71
	s_nop 1
	v_mov_b32_dpp v73, v73 quad_perm:[1,0,3,2] row_mask:0xf bank_mask:0xf
	s_waitcnt lgkmcnt(0)
	v_fmac_f32_e32 v73, v69, v71
	s_nop 1
	v_mov_b32_dpp v69, v73 quad_perm:[2,3,0,1] row_mask:0xf bank_mask:0xf
	s_waitcnt lgkmcnt(0)
	v_add_f32_e32 v69, v73, v69
	s_nop 1
	v_mov_b32_dpp v71, v69 row_half_mirror row_mask:0xf bank_mask:0xf
	s_waitcnt lgkmcnt(0)
	v_add_f32_e32 v69, v69, v71
	s_nop 1
	v_mov_b32_dpp v71, v69 row_mirror row_mask:0xf bank_mask:0xf
	s_waitcnt lgkmcnt(0)
	v_add_f32_e32 v69, v69, v71
	ds_bpermute_b32 v71, v1, v69
	s_waitcnt lgkmcnt(0)
	v_add_f32_e32 v69, v69, v71
	ds_bpermute_b32 v71, v143, v69
	s_waitcnt lgkmcnt(0)
	v_add_f32_e32 v69, v69, v71
	v_mul_f32_e32 v71, 0x3fb8aa3b, v69
	v_fma_f32 v73, v69, s10, -v71
	v_rndne_f32_e32 v75, v71
	v_fmac_f32_e32 v73, 0x32a5705f, v69
	v_sub_f32_e32 v71, v71, v75
	v_add_f32_e32 v71, v71, v73
	v_exp_f32_e32 v71, v71
	v_cvt_i32_f32_e32 v73, v75
	v_cmp_ngt_f32_e32 vcc, s11, v69
	v_ldexp_f32 v71, v71, v73
	s_nop 0
	v_cndmask_b32_e32 v71, 0, v71, vcc
	v_cmp_nlt_f32_e32 vcc, s12, v69
	s_nop 1
	v_cndmask_b32_e32 v69, v237, v71, vcc
	v_mov_b32_e32 v71, v250
	v_mov_b32_e32 v73, v251
	ds_read2_b32 v[100:101], v67 offset1:32
	v_mul_f32_e32 v75, v71, v73
	s_nop 1
	v_mov_b32_dpp v75, v75 quad_perm:[1,0,3,2] row_mask:0xf bank_mask:0xf
	s_waitcnt lgkmcnt(0)
	v_fmac_f32_e32 v75, v71, v73
	s_nop 1
	v_mov_b32_dpp v71, v75 quad_perm:[2,3,0,1] row_mask:0xf bank_mask:0xf
	s_waitcnt lgkmcnt(0)
	v_add_f32_e32 v71, v75, v71
	s_nop 1
	v_mov_b32_dpp v73, v71 row_half_mirror row_mask:0xf bank_mask:0xf
	s_waitcnt lgkmcnt(0)
	v_add_f32_e32 v71, v71, v73
	s_nop 1
	v_mov_b32_dpp v73, v71 row_mirror row_mask:0xf bank_mask:0xf
	s_waitcnt lgkmcnt(0)
	v_add_f32_e32 v71, v71, v73
	ds_bpermute_b32 v73, v1, v71
	s_waitcnt lgkmcnt(0)
	v_add_f32_e32 v71, v71, v73
	ds_bpermute_b32 v73, v143, v71
	s_waitcnt lgkmcnt(0)
	v_add_f32_e32 v71, v71, v73
	v_mul_f32_e32 v73, 0x3fb8aa3b, v71
	v_fma_f32 v75, v71, s10, -v73
	v_rndne_f32_e32 v77, v73
	v_fmac_f32_e32 v75, 0x32a5705f, v71
	v_sub_f32_e32 v73, v73, v77
	v_add_f32_e32 v73, v73, v75
	v_exp_f32_e32 v73, v73
	v_cvt_i32_f32_e32 v75, v77
	v_cmp_ngt_f32_e32 vcc, s11, v71
	v_ldexp_f32 v73, v73, v75
	s_nop 0
	v_cndmask_b32_e32 v73, 0, v73, vcc
	v_cmp_nlt_f32_e32 vcc, s12, v71
	v_ashrrev_i32_e32 v75, 31, v74
	v_lshlrev_b64 v[74:75], 11, v[74:75]
	v_cndmask_b32_e32 v71, v237, v73, vcc
	v_sub_f32_e32 v69, v69, v71
	v_add_f32_e32 v116, s5, v69
	v_pk_mul_f32 v[100:101], v[100:101], v[116:117] op_sel_hi:[1,0]
	v_sub_f32_e64 v69, 1.0, s5
	v_pk_fma_f32 v[100:101], v[102:103], v[76:77], v[100:101] op_sel_hi:[1,0,1] neg_lo:[0,0,1] neg_hi:[0,0,1]
	ds_read2_b32 v[102:103], v67 offset0:64 offset1:96
	v_pk_mul_f32 v[144:145], v[100:101], v[100:101]
	v_add_u32_e32 v71, 0x400, v67
	v_readlane_b32 s5, v254, 61
	v_ashrrev_i32_e32 v73, 31, v72
	s_waitcnt lgkmcnt(0)
	v_mov_b32_e32 v148, v103
	v_mov_b32_e32 v149, v102
	v_pk_mul_f32 v[102:103], v[116:117], v[148:149] op_sel_hi:[0,1]
	v_pk_fma_f32 v[76:77], v[146:147], v[76:77], v[102:103] op_sel_hi:[1,0,1] neg_lo:[0,0,1] neg_hi:[0,0,1]
	ds_read2_b32 v[102:103], v67 offset0:128 offset1:160
	v_pk_mul_f32 v[146:147], v[76:77], v[76:77]
	v_lshlrev_b64 v[72:73], 11, v[72:73]
	s_waitcnt lgkmcnt(0)
	v_pk_mul_f32 v[2:3], v[116:117], v[102:103] op_sel_hi:[0,1]
	v_pk_fma_f32 v[102:103], v[18:19], v[122:123], v[2:3] op_sel_hi:[1,0,1] neg_lo:[0,0,1] neg_hi:[0,0,1]
	ds_read2_b32 v[2:3], v67 offset0:192 offset1:224
	v_pk_mul_f32 v[18:19], v[102:103], v[102:103]
	s_waitcnt lgkmcnt(0)
; __device__ __forceinline__ int crow(int r, int hi) { return (r & 3) + 8 * (r >> 2) + 4 * hi; }
; __device__ __forceinline__ void diff_unit(KP Pk, Frame& F, int l, int b, int h, int qrow0, int nkt) {
;     ...
;         float ssq[16];
; #pragma unroll
;         for (int r = 0; r < 16; ++r) { float a = 0.f;
; #pragma unroll
;             for (int nb = 0; nb < 4; ++nb) { const float v = O[nb][r] * rlr[r] - lam * ex[crow(r, hi) * 128 + nb * 32 + r32]; O[nb][r] = v; a += v * v; }
;             a += __shfl_xor(a, 1); a += __shfl_xor(a, 2); a += __shfl_xor(a, 4); a += __shfl_xor(a, 8); a += __shfl_xor(a, 16);
;             ssq[r] = rsqrtf(a * (1.f / 128.f) + NORM_EPS) * (1.f - lam_init); }
	v_pk_mul_f32 v[2:3], v[116:117], v[2:3] op_sel_hi:[0,1]
	v_pk_fma_f32 v[2:3], v[50:51], v[122:123], v[2:3] op_sel_hi:[1,0,1] neg_lo:[0,0,1] neg_hi:[0,0,1]
	v_mov_b32_e32 v50, v18
	v_pk_mul_f32 v[34:35], v[2:3], v[2:3]
	v_mov_b32_e32 v51, v144
	v_mov_b32_e32 v144, v19
	v_pk_add_f32 v[18:19], v[50:51], v[144:145]
	v_mov_b32_e32 v50, v34
	v_mov_b32_e32 v51, v147
	v_pk_add_f32 v[18:19], v[18:19], v[50:51]
	v_pk_mov_b32 v[34:35], v[34:35], v[146:147] op_sel:[1,0]
	v_mov_b64_e32 v[122:123], s[8:9]
	v_pk_add_f32 v[18:19], v[18:19], v[34:35]
	s_nop 1
	v_mov_b32_dpp v35, v19 quad_perm:[1,0,3,2] row_mask:0xf bank_mask:0xf
	v_mov_b32_dpp v34, v18 quad_perm:[1,0,3,2] row_mask:0xf bank_mask:0xf
	s_brev_b32 s8, 60
	ds_read2_b32 v[146:147], v71 offset0:128 offset1:160
	v_mov_b32_e32 v144, v36
	v_mov_b32_e32 v145, v52
	s_waitcnt lgkmcnt(0)
	v_pk_add_f32 v[18:19], v[18:19], v[34:35]
	s_nop 1
	v_mov_b32_dpp v35, v19 quad_perm:[2,3,0,1] row_mask:0xf bank_mask:0xf
	v_mov_b32_dpp v34, v18 quad_perm:[2,3,0,1] row_mask:0xf bank_mask:0xf
	v_mov_b32_e32 v52, v37
	s_waitcnt lgkmcnt(0)
	v_pk_add_f32 v[18:19], v[18:19], v[34:35]
	s_nop 1
	v_mov_b32_dpp v35, v19 row_half_mirror row_mask:0xf bank_mask:0xf
	v_mov_b32_dpp v34, v18 row_half_mirror row_mask:0xf bank_mask:0xf
	s_waitcnt lgkmcnt(0)
	v_pk_add_f32 v[18:19], v[18:19], v[34:35]
	s_nop 1
	v_mov_b32_dpp v35, v19 row_mirror row_mask:0xf bank_mask:0xf
	v_mov_b32_dpp v34, v18 row_mirror row_mask:0xf bank_mask:0xf
	s_waitcnt lgkmcnt(0)
	v_pk_add_f32 v[18:19], v[18:19], v[34:35]
	ds_bpermute_b32 v35, v1, v19
	ds_bpermute_b32 v34, v1, v18
	s_waitcnt lgkmcnt(0)
	v_pk_add_f32 v[18:19], v[18:19], v[34:35]
	s_nop 0
	v_pk_fma_f32 v[18:19], v[18:19], s[8:9], v[122:123] op_sel_hi:[1,0,0]
	v_mov_b32_e32 v35, v20
	v_mul_f32_e32 v34, 0x4b800000, v19
	v_cmp_gt_f32_e64 s[38:39], s66, v19
	v_cmp_gt_f32_e32 vcc, s66, v18
	v_mov_b32_e32 v20, v5
	v_cndmask_b32_e64 v19, v19, v34, s[38:39]
	v_rsq_f32_e32 v19, v19
	s_nop 0
	v_mul_f32_e32 v34, 0x45800000, v19
	v_cndmask_b32_e64 v19, v19, v34, s[38:39]
	v_mul_f32_e32 v111, v69, v19
	v_mul_f32_e32 v19, 0x4b800000, v18
	v_cndmask_b32_e32 v18, v18, v19, vcc
	v_rsq_f32_e32 v18, v18
	v_mov_b32_e32 v34, v4
	v_pk_mul_f32 v[4:5], v[116:117], v[146:147] op_sel_hi:[0,1]
	v_pk_fma_f32 v[20:21], v[20:21], v[136:137], v[4:5] op_sel_hi:[1,0,1] neg_lo:[0,0,1] neg_hi:[0,0,1]
	v_mul_f32_e32 v19, 0x45800000, v18
	v_cndmask_b32_e32 v18, v18, v19, vcc
	v_mul_f32_e32 v109, v69, v18
	ds_read2_b32 v[18:19], v71 offset1:32
	ds_read2_b32 v[4:5], v71 offset0:192 offset1:224
	v_pk_mul_f32 v[146:147], v[20:21], v[20:21]
	v_mul_f32_e32 v2, v2, v109
	v_mul_f32_e32 v3, v3, v109
	s_waitcnt lgkmcnt(0)
	v_pk_mul_f32 v[18:19], v[116:117], v[18:19] op_sel_hi:[0,1]
	v_pk_fma_f32 v[34:35], v[34:35], v[138:139], v[18:19] op_sel_hi:[1,0,1] neg_lo:[0,0,1] neg_hi:[0,0,1]
	ds_read2_b32 v[18:19], v71 offset0:64 offset1:96
	s_waitcnt lgkmcnt(0)
	v_pk_mul_f32 v[4:5], v[116:117], v[4:5] op_sel_hi:[0,1]
	v_pk_mul_f32 v[50:51], v[34:35], v[34:35]
	v_pk_fma_f32 v[4:5], v[52:53], v[136:137], v[4:5] op_sel_hi:[1,0,1] neg_lo:[0,0,1] neg_hi:[0,0,1]
	v_mov_b32_e32 v52, v146
	s_waitcnt lgkmcnt(0)
	v_pk_mul_f32 v[18:19], v[116:117], v[18:19] op_sel_hi:[0,1]
	v_pk_fma_f32 v[18:19], v[144:145], v[138:139], v[18:19] op_sel_hi:[1,0,1] neg_lo:[0,0,1] neg_hi:[0,0,1]
	v_pk_mul_f32 v[36:37], v[4:5], v[4:5]
	v_pk_mul_f32 v[144:145], v[18:19], v[18:19]
	v_mov_b32_e32 v53, v50
	v_mov_b32_e32 v50, v147
	v_pk_add_f32 v[50:51], v[52:53], v[50:51]
	v_mov_b32_e32 v52, v36
	v_mov_b32_e32 v53, v144
	v_pk_add_f32 v[50:51], v[50:51], v[52:53]
	v_mov_b32_e32 v144, v37
	v_pk_add_f32 v[36:37], v[50:51], v[144:145]
	s_nop 1
	v_mov_b32_dpp v51, v37 quad_perm:[1,0,3,2] row_mask:0xf bank_mask:0xf
	v_mov_b32_dpp v50, v36 quad_perm:[1,0,3,2] row_mask:0xf bank_mask:0xf
	v_add_u32_e32 v71, 0x1000, v67
	v_mov_b32_e32 v52, v38
	v_mov_b32_e32 v53, v54
	v_mov_b32_e32 v54, v39
	s_waitcnt lgkmcnt(0)
	v_pk_add_f32 v[36:37], v[36:37], v[50:51]
	s_nop 1
	v_mov_b32_dpp v51, v37 quad_perm:[2,3,0,1] row_mask:0xf bank_mask:0xf
	v_mov_b32_dpp v50, v36 quad_perm:[2,3,0,1] row_mask:0xf bank_mask:0xf
	s_waitcnt lgkmcnt(0)
	v_pk_add_f32 v[36:37], v[36:37], v[50:51]
	s_nop 1
	v_mov_b32_dpp v51, v37 row_half_mirror row_mask:0xf bank_mask:0xf
	v_mov_b32_dpp v50, v36 row_half_mirror row_mask:0xf bank_mask:0xf
	s_waitcnt lgkmcnt(0)
	v_pk_add_f32 v[36:37], v[36:37], v[50:51]
	s_nop 1
	v_mov_b32_dpp v51, v37 row_mirror row_mask:0xf bank_mask:0xf
	v_mov_b32_dpp v50, v36 row_mirror row_mask:0xf bank_mask:0xf
	s_waitcnt lgkmcnt(0)
	v_pk_add_f32 v[36:37], v[36:37], v[50:51]
	ds_bpermute_b32 v51, v1, v37
	ds_bpermute_b32 v50, v1, v36
	s_waitcnt lgkmcnt(0)
	v_pk_add_f32 v[36:37], v[36:37], v[50:51]
	s_nop 0
	v_pk_fma_f32 v[36:37], v[36:37], s[8:9], v[122:123] op_sel_hi:[1,0,0]
	v_mov_b32_e32 v51, v22
	v_mul_f32_e32 v50, 0x4b800000, v37
	v_cmp_gt_f32_e64 s[38:39], s66, v37
	v_cmp_gt_f32_e32 vcc, s66, v36
	v_mov_b32_e32 v22, v7
	v_cndmask_b32_e64 v37, v37, v50, s[38:39]
	v_rsq_f32_e32 v37, v37
	s_nop 0
	v_mul_f32_e32 v50, 0x45800000, v37
	v_cndmask_b32_e64 v37, v37, v50, s[38:39]
	v_mul_f32_e32 v115, v69, v37
	v_mul_f32_e32 v37, 0x4b800000, v36
	v_cndmask_b32_e32 v36, v36, v37, vcc
	v_rsq_f32_e32 v36, v36
	v_mov_b32_e32 v50, v6
	v_mul_f32_e32 v34, v34, v115
	v_mul_f32_e32 v37, 0x45800000, v36
	v_cndmask_b32_e32 v36, v36, v37, vcc
	v_mul_f32_e32 v113, v69, v36
	ds_read2_b32 v[36:37], v71 offset1:32
	v_mul_f32_e32 v20, v20, v113
	v_mul_f32_e32 v21, v21, v113
	s_waitcnt lgkmcnt(0)
; __device__ __forceinline__ int crow(int r, int hi) { return (r & 3) + 8 * (r >> 2) + 4 * hi; }
; __device__ __forceinline__ void diff_unit(KP Pk, Frame& F, int l, int b, int h, int qrow0, int nkt) {
;     ...
;         float ssq[16];
; #pragma unroll
;         for (int r = 0; r < 16; ++r) { float a = 0.f;
; #pragma unroll
;             for (int nb = 0; nb < 4; ++nb) { const float v = O[nb][r] * rlr[r] - lam * ex[crow(r, hi) * 128 + nb * 32 + r32]; O[nb][r] = v; a += v * v; }
;             a += __shfl_xor(a, 1); a += __shfl_xor(a, 2); a += __shfl_xor(a, 4); a += __shfl_xor(a, 8); a += __shfl_xor(a, 16);
;             ssq[r] = rsqrtf(a * (1.f / 128.f) + NORM_EPS) * (1.f - lam_init); }
	v_pk_mul_f32 v[36:37], v[116:117], v[36:37] op_sel_hi:[0,1]
	v_pk_fma_f32 v[36:37], v[50:51], v[134:135], v[36:37] op_sel_hi:[1,0,1] neg_lo:[0,0,1] neg_hi:[0,0,1]
	ds_read2_b32 v[50:51], v71 offset0:64 offset1:96
	v_pk_mul_f32 v[136:137], v[36:37], v[36:37]
	s_waitcnt lgkmcnt(0)
	v_pk_mul_f32 v[50:51], v[116:117], v[50:51] op_sel_hi:[0,1]
	v_pk_fma_f32 v[50:51], v[52:53], v[134:135], v[50:51] op_sel_hi:[1,0,1] neg_lo:[0,0,1] neg_hi:[0,0,1]
	ds_read2_b32 v[52:53], v71 offset0:128 offset1:160
	v_pk_mul_f32 v[134:135], v[50:51], v[50:51]
	s_waitcnt lgkmcnt(0)
	v_pk_mul_f32 v[6:7], v[116:117], v[52:53] op_sel_hi:[0,1]
	v_pk_fma_f32 v[52:53], v[22:23], v[132:133], v[6:7] op_sel_hi:[1,0,1] neg_lo:[0,0,1] neg_hi:[0,0,1]
	ds_read2_b32 v[6:7], v71 offset0:192 offset1:224
	v_pk_mul_f32 v[22:23], v[52:53], v[52:53]
	v_add_u32_e32 v71, 0x1400, v67
	s_waitcnt lgkmcnt(0)
	v_pk_mul_f32 v[6:7], v[116:117], v[6:7] op_sel_hi:[0,1]
	v_pk_fma_f32 v[6:7], v[54:55], v[132:133], v[6:7] op_sel_hi:[1,0,1] neg_lo:[0,0,1] neg_hi:[0,0,1]
	v_mov_b32_e32 v54, v22
	v_pk_mul_f32 v[38:39], v[6:7], v[6:7]
	v_mov_b32_e32 v55, v136
	v_mov_b32_e32 v136, v23
	v_pk_add_f32 v[22:23], v[54:55], v[136:137]
	v_mov_b32_e32 v54, v38
	v_mov_b32_e32 v55, v134
	v_pk_add_f32 v[22:23], v[22:23], v[54:55]
	v_mov_b32_e32 v134, v39
	v_pk_add_f32 v[22:23], v[22:23], v[134:135]
	s_nop 1
	v_mov_b32_dpp v39, v23 quad_perm:[1,0,3,2] row_mask:0xf bank_mask:0xf
	v_mov_b32_dpp v38, v22 quad_perm:[1,0,3,2] row_mask:0xf bank_mask:0xf
	v_mov_b32_e32 v54, v40
	v_mov_b32_e32 v55, v56
	v_mov_b32_e32 v56, v41
	s_waitcnt lgkmcnt(0)
	v_pk_add_f32 v[22:23], v[22:23], v[38:39]
	s_nop 1
	v_mov_b32_dpp v39, v23 quad_perm:[2,3,0,1] row_mask:0xf bank_mask:0xf
	v_mov_b32_dpp v38, v22 quad_perm:[2,3,0,1] row_mask:0xf bank_mask:0xf
	s_waitcnt lgkmcnt(0)
	v_pk_add_f32 v[22:23], v[22:23], v[38:39]
	s_nop 1
	v_mov_b32_dpp v39, v23 row_half_mirror row_mask:0xf bank_mask:0xf
	v_mov_b32_dpp v38, v22 row_half_mirror row_mask:0xf bank_mask:0xf
	s_waitcnt lgkmcnt(0)
	v_pk_add_f32 v[22:23], v[22:23], v[38:39]
	s_nop 1
	v_mov_b32_dpp v39, v23 row_mirror row_mask:0xf bank_mask:0xf
	v_mov_b32_dpp v38, v22 row_mirror row_mask:0xf bank_mask:0xf
	s_waitcnt lgkmcnt(0)
	v_pk_add_f32 v[22:23], v[22:23], v[38:39]
	ds_bpermute_b32 v39, v1, v23
	ds_bpermute_b32 v38, v1, v22
	s_waitcnt lgkmcnt(0)
	v_pk_add_f32 v[22:23], v[22:23], v[38:39]
	s_nop 0
	v_pk_fma_f32 v[22:23], v[22:23], s[8:9], v[122:123] op_sel_hi:[1,0,0]
	v_mov_b32_e32 v39, v24
	v_mul_f32_e32 v38, 0x4b800000, v23
	v_cmp_gt_f32_e64 s[38:39], s66, v23
	v_cmp_gt_f32_e32 vcc, s66, v22
	v_mov_b32_e32 v24, v9
	v_cndmask_b32_e64 v23, v23, v38, s[38:39]
	v_rsq_f32_e32 v23, v23
	s_nop 0
	v_mul_f32_e32 v38, 0x45800000, v23
	v_cndmask_b32_e64 v23, v23, v38, s[38:39]
	v_mul_f32_e32 v119, v69, v23
	v_mul_f32_e32 v23, 0x4b800000, v22
	v_cndmask_b32_e32 v22, v22, v23, vcc
	v_rsq_f32_e32 v22, v22
	v_mov_b32_e32 v38, v8
	v_mul_f32_e32 v23, 0x45800000, v22
	v_cndmask_b32_e32 v22, v22, v23, vcc
	v_mul_f32_e32 v117, v69, v22
	ds_read2_b32 v[22:23], v71 offset1:32
	s_waitcnt lgkmcnt(0)
	v_pk_mul_f32 v[22:23], v[116:117], v[22:23] op_sel_hi:[0,1]
	v_pk_fma_f32 v[38:39], v[38:39], v[130:131], v[22:23] op_sel_hi:[1,0,1] neg_lo:[0,0,1] neg_hi:[0,0,1]
	ds_read2_b32 v[22:23], v71 offset0:64 offset1:96
	v_pk_mul_f32 v[132:133], v[38:39], v[38:39]
	s_waitcnt lgkmcnt(0)
	v_pk_mul_f32 v[22:23], v[116:117], v[22:23] op_sel_hi:[0,1]
	v_pk_fma_f32 v[22:23], v[54:55], v[130:131], v[22:23] op_sel_hi:[1,0,1] neg_lo:[0,0,1] neg_hi:[0,0,1]
	ds_read2_b32 v[54:55], v71 offset0:128 offset1:160
	v_pk_mul_f32 v[130:131], v[22:23], v[22:23]
	s_waitcnt lgkmcnt(0)
	v_pk_mul_f32 v[8:9], v[116:117], v[54:55] op_sel_hi:[0,1]
	v_pk_fma_f32 v[54:55], v[24:25], v[128:129], v[8:9] op_sel_hi:[1,0,1] neg_lo:[0,0,1] neg_hi:[0,0,1]
	ds_read2_b32 v[8:9], v71 offset0:192 offset1:224
	v_pk_mul_f32 v[24:25], v[54:55], v[54:55]
	v_add_u32_e32 v71, 0x2000, v67
	s_waitcnt lgkmcnt(0)
	v_pk_mul_f32 v[8:9], v[116:117], v[8:9] op_sel_hi:[0,1]
	v_pk_fma_f32 v[8:9], v[56:57], v[128:129], v[8:9] op_sel_hi:[1,0,1] neg_lo:[0,0,1] neg_hi:[0,0,1]
	v_mov_b32_e32 v56, v24
	v_pk_mul_f32 v[40:41], v[8:9], v[8:9]
	v_mov_b32_e32 v57, v132
	v_mov_b32_e32 v132, v25
	v_pk_add_f32 v[24:25], v[56:57], v[132:133]
	v_mov_b32_e32 v56, v40
	v_mov_b32_e32 v57, v130
	v_pk_add_f32 v[24:25], v[24:25], v[56:57]
	v_mov_b32_e32 v130, v41
	v_pk_add_f32 v[24:25], v[24:25], v[130:131]
	s_nop 1
	v_mov_b32_dpp v41, v25 quad_perm:[1,0,3,2] row_mask:0xf bank_mask:0xf
	v_mov_b32_dpp v40, v24 quad_perm:[1,0,3,2] row_mask:0xf bank_mask:0xf
	v_mov_b32_e32 v56, v42
	v_mov_b32_e32 v57, v58
	v_mov_b32_e32 v58, v43
	s_waitcnt lgkmcnt(0)
	v_pk_add_f32 v[24:25], v[24:25], v[40:41]
	s_nop 1
	v_mov_b32_dpp v41, v25 quad_perm:[2,3,0,1] row_mask:0xf bank_mask:0xf
	v_mov_b32_dpp v40, v24 quad_perm:[2,3,0,1] row_mask:0xf bank_mask:0xf
	s_waitcnt lgkmcnt(0)
	v_pk_add_f32 v[24:25], v[24:25], v[40:41]
	s_nop 1
	v_mov_b32_dpp v41, v25 row_half_mirror row_mask:0xf bank_mask:0xf
	v_mov_b32_dpp v40, v24 row_half_mirror row_mask:0xf bank_mask:0xf
	s_waitcnt lgkmcnt(0)
	v_pk_add_f32 v[24:25], v[24:25], v[40:41]
	s_nop 1
	v_mov_b32_dpp v41, v25 row_mirror row_mask:0xf bank_mask:0xf
	v_mov_b32_dpp v40, v24 row_mirror row_mask:0xf bank_mask:0xf
	s_waitcnt lgkmcnt(0)
	v_pk_add_f32 v[24:25], v[24:25], v[40:41]
	ds_bpermute_b32 v41, v1, v25
	ds_bpermute_b32 v40, v1, v24
	s_waitcnt lgkmcnt(0)
; __device__ __forceinline__ int crow(int r, int hi) { return (r & 3) + 8 * (r >> 2) + 4 * hi; }
; __device__ __forceinline__ void diff_unit(KP Pk, Frame& F, int l, int b, int h, int qrow0, int nkt) {
;     ...
;         float ssq[16];
; #pragma unroll
;         for (int r = 0; r < 16; ++r) { float a = 0.f;
; #pragma unroll
;             for (int nb = 0; nb < 4; ++nb) { const float v = O[nb][r] * rlr[r] - lam * ex[crow(r, hi) * 128 + nb * 32 + r32]; O[nb][r] = v; a += v * v; }
;             a += __shfl_xor(a, 1); a += __shfl_xor(a, 2); a += __shfl_xor(a, 4); a += __shfl_xor(a, 8); a += __shfl_xor(a, 16);
;             ssq[r] = rsqrtf(a * (1.f / 128.f) + NORM_EPS) * (1.f - lam_init); }
	v_pk_add_f32 v[24:25], v[24:25], v[40:41]
	s_nop 0
	v_pk_fma_f32 v[24:25], v[24:25], s[8:9], v[122:123] op_sel_hi:[1,0,0]
	v_mov_b32_e32 v41, v26
	v_mul_f32_e32 v40, 0x4b800000, v25
	v_cmp_gt_f32_e64 s[38:39], s66, v25
	v_cmp_gt_f32_e32 vcc, s66, v24
	v_mov_b32_e32 v26, v11
	v_cndmask_b32_e64 v25, v25, v40, s[38:39]
	v_rsq_f32_e32 v25, v25
	s_nop 0
	v_mul_f32_e32 v40, 0x45800000, v25
	v_cndmask_b32_e64 v25, v25, v40, s[38:39]
	v_mul_f32_e32 v125, v69, v25
	v_mul_f32_e32 v25, 0x4b800000, v24
	v_cndmask_b32_e32 v24, v24, v25, vcc
	v_rsq_f32_e32 v24, v24
	v_mov_b32_e32 v40, v10
	v_mul_f32_e32 v25, 0x45800000, v24
	v_cndmask_b32_e32 v24, v24, v25, vcc
	v_mul_f32_e32 v121, v69, v24
	ds_read2_b32 v[24:25], v71 offset1:32
	s_waitcnt lgkmcnt(0)
	v_pk_mul_f32 v[24:25], v[116:117], v[24:25] op_sel_hi:[0,1]
	v_pk_fma_f32 v[40:41], v[40:41], v[126:127], v[24:25] op_sel_hi:[1,0,1] neg_lo:[0,0,1] neg_hi:[0,0,1]
	ds_read2_b32 v[24:25], v71 offset0:64 offset1:96
	v_pk_mul_f32 v[128:129], v[40:41], v[40:41]
	s_waitcnt lgkmcnt(0)
	v_pk_mul_f32 v[24:25], v[116:117], v[24:25] op_sel_hi:[0,1]
	v_pk_fma_f32 v[24:25], v[56:57], v[126:127], v[24:25] op_sel_hi:[1,0,1] neg_lo:[0,0,1] neg_hi:[0,0,1]
	ds_read2_b32 v[56:57], v71 offset0:128 offset1:160
	v_pk_mul_f32 v[126:127], v[24:25], v[24:25]
	s_waitcnt lgkmcnt(0)
	v_pk_mul_f32 v[10:11], v[116:117], v[56:57] op_sel_hi:[0,1]
	v_pk_fma_f32 v[56:57], v[26:27], v[124:125], v[10:11] op_sel_hi:[1,0,1] neg_lo:[0,0,1] neg_hi:[0,0,1]
	ds_read2_b32 v[10:11], v71 offset0:192 offset1:224
	v_pk_mul_f32 v[26:27], v[56:57], v[56:57]
	v_add_u32_e32 v71, 0x2400, v67
	s_waitcnt lgkmcnt(0)
	v_pk_mul_f32 v[10:11], v[116:117], v[10:11] op_sel_hi:[0,1]
	v_pk_fma_f32 v[10:11], v[58:59], v[124:125], v[10:11] op_sel_hi:[1,0,1] neg_lo:[0,0,1] neg_hi:[0,0,1]
	v_mov_b32_e32 v58, v26
	v_pk_mul_f32 v[42:43], v[10:11], v[10:11]
	v_mov_b32_e32 v59, v128
	v_mov_b32_e32 v128, v27
	v_pk_add_f32 v[26:27], v[58:59], v[128:129]
	v_mov_b32_e32 v58, v42
	v_mov_b32_e32 v59, v126
	v_pk_add_f32 v[26:27], v[26:27], v[58:59]
	v_mov_b32_e32 v126, v43
	v_pk_add_f32 v[26:27], v[26:27], v[126:127]
	s_nop 1
	v_mov_b32_dpp v43, v27 quad_perm:[1,0,3,2] row_mask:0xf bank_mask:0xf
	v_mov_b32_dpp v42, v26 quad_perm:[1,0,3,2] row_mask:0xf bank_mask:0xf
	v_mov_b32_e32 v58, v44
	v_mov_b32_e32 v59, v60
	v_mov_b32_e32 v60, v45
	s_waitcnt lgkmcnt(0)
	v_pk_add_f32 v[26:27], v[26:27], v[42:43]
	s_nop 1
	v_mov_b32_dpp v43, v27 quad_perm:[2,3,0,1] row_mask:0xf bank_mask:0xf
	v_mov_b32_dpp v42, v26 quad_perm:[2,3,0,1] row_mask:0xf bank_mask:0xf
	s_waitcnt lgkmcnt(0)
	v_pk_add_f32 v[26:27], v[26:27], v[42:43]
	s_nop 1
	v_mov_b32_dpp v43, v27 row_half_mirror row_mask:0xf bank_mask:0xf
	v_mov_b32_dpp v42, v26 row_half_mirror row_mask:0xf bank_mask:0xf
	s_waitcnt lgkmcnt(0)
	v_pk_add_f32 v[26:27], v[26:27], v[42:43]
	s_nop 1
	v_mov_b32_dpp v43, v27 row_mirror row_mask:0xf bank_mask:0xf
	v_mov_b32_dpp v42, v26 row_mirror row_mask:0xf bank_mask:0xf
	s_waitcnt lgkmcnt(0)
	v_pk_add_f32 v[26:27], v[26:27], v[42:43]
	ds_bpermute_b32 v43, v1, v27
	ds_bpermute_b32 v42, v1, v26
	s_waitcnt lgkmcnt(0)
	v_pk_add_f32 v[26:27], v[26:27], v[42:43]
	s_nop 0
	v_pk_fma_f32 v[26:27], v[26:27], s[8:9], v[122:123] op_sel_hi:[1,0,0]
	v_mov_b32_e32 v43, v28
	v_mul_f32_e32 v42, 0x4b800000, v27
	v_cmp_gt_f32_e64 s[38:39], s66, v27
	v_cmp_gt_f32_e32 vcc, s66, v26
	v_mov_b32_e32 v28, v13
	v_cndmask_b32_e64 v27, v27, v42, s[38:39]
	v_rsq_f32_e32 v27, v27
	s_nop 0
	v_mul_f32_e32 v42, 0x45800000, v27
	v_cndmask_b32_e64 v27, v27, v42, s[38:39]
	v_mul_f32_e32 v126, v69, v27
	v_mul_f32_e32 v27, 0x4b800000, v26
	v_cndmask_b32_e32 v26, v26, v27, vcc
	v_rsq_f32_e32 v26, v26
	v_mov_b32_e32 v42, v12
	v_mul_f32_e32 v27, 0x45800000, v26
	v_cndmask_b32_e32 v26, v26, v27, vcc
	v_mul_f32_e32 v124, v69, v26
	ds_read2_b32 v[26:27], v71 offset1:32
	s_waitcnt lgkmcnt(0)
	v_pk_mul_f32 v[26:27], v[116:117], v[26:27] op_sel_hi:[0,1]
	v_pk_fma_f32 v[42:43], v[42:43], v[120:121], v[26:27] op_sel_hi:[1,0,1] neg_lo:[0,0,1] neg_hi:[0,0,1]
	ds_read2_b32 v[26:27], v71 offset0:64 offset1:96
	v_pk_mul_f32 v[128:129], v[42:43], v[42:43]
	s_waitcnt lgkmcnt(0)
	v_pk_mul_f32 v[26:27], v[116:117], v[26:27] op_sel_hi:[0,1]
	v_pk_fma_f32 v[26:27], v[58:59], v[120:121], v[26:27] op_sel_hi:[1,0,1] neg_lo:[0,0,1] neg_hi:[0,0,1]
	ds_read2_b32 v[58:59], v71 offset0:128 offset1:160
	v_pk_mul_f32 v[130:131], v[26:27], v[26:27]
	s_waitcnt lgkmcnt(0)
	v_pk_mul_f32 v[12:13], v[116:117], v[58:59] op_sel_hi:[0,1]
	v_pk_fma_f32 v[58:59], v[28:29], v[118:119], v[12:13] op_sel_hi:[1,0,1] neg_lo:[0,0,1] neg_hi:[0,0,1]
	ds_read2_b32 v[12:13], v71 offset0:192 offset1:224
	v_pk_mul_f32 v[28:29], v[58:59], v[58:59]
	v_add_u32_e32 v71, 0x3000, v67
	v_add_u32_e32 v67, 0x3400, v67
	s_waitcnt lgkmcnt(0)
	v_pk_mul_f32 v[12:13], v[116:117], v[12:13] op_sel_hi:[0,1]
	v_pk_fma_f32 v[12:13], v[60:61], v[118:119], v[12:13] op_sel_hi:[1,0,1] neg_lo:[0,0,1] neg_hi:[0,0,1]
	v_mov_b32_e32 v60, v28
	v_pk_mul_f32 v[44:45], v[12:13], v[12:13]
	v_mov_b32_e32 v61, v128
	v_mov_b32_e32 v128, v29
	v_pk_add_f32 v[28:29], v[60:61], v[128:129]
	v_mov_b32_e32 v60, v44
	v_mov_b32_e32 v61, v130
	v_pk_add_f32 v[28:29], v[28:29], v[60:61]
	v_mov_b32_e32 v130, v45
	v_pk_add_f32 v[28:29], v[28:29], v[130:131]
	s_nop 1
	v_mov_b32_dpp v45, v29 quad_perm:[1,0,3,2] row_mask:0xf bank_mask:0xf
	v_mov_b32_dpp v44, v28 quad_perm:[1,0,3,2] row_mask:0xf bank_mask:0xf
	v_mov_b32_e32 v60, v46
	v_mov_b32_e32 v61, v62
	v_mov_b32_e32 v62, v47
	s_waitcnt lgkmcnt(0)
	v_pk_add_f32 v[28:29], v[28:29], v[44:45]
	s_nop 1
	v_mov_b32_dpp v45, v29 quad_perm:[2,3,0,1] row_mask:0xf bank_mask:0xf
	v_mov_b32_dpp v44, v28 quad_perm:[2,3,0,1] row_mask:0xf bank_mask:0xf
	s_waitcnt lgkmcnt(0)
; __device__ __forceinline__ int crow(int r, int hi) { return (r & 3) + 8 * (r >> 2) + 4 * hi; }
; __device__ __forceinline__ void diff_unit(KP Pk, Frame& F, int l, int b, int h, int qrow0, int nkt) {
;     ...
;         float ssq[16];
; #pragma unroll
;         for (int r = 0; r < 16; ++r) { float a = 0.f;
; #pragma unroll
;             for (int nb = 0; nb < 4; ++nb) { const float v = O[nb][r] * rlr[r] - lam * ex[crow(r, hi) * 128 + nb * 32 + r32]; O[nb][r] = v; a += v * v; }
;             a += __shfl_xor(a, 1); a += __shfl_xor(a, 2); a += __shfl_xor(a, 4); a += __shfl_xor(a, 8); a += __shfl_xor(a, 16);
;             ssq[r] = rsqrtf(a * (1.f / 128.f) + NORM_EPS) * (1.f - lam_init); }
	v_pk_add_f32 v[28:29], v[28:29], v[44:45]
	s_nop 1
	v_mov_b32_dpp v45, v29 row_half_mirror row_mask:0xf bank_mask:0xf
	v_mov_b32_dpp v44, v28 row_half_mirror row_mask:0xf bank_mask:0xf
	s_waitcnt lgkmcnt(0)
	v_pk_add_f32 v[28:29], v[28:29], v[44:45]
	s_nop 1
	v_mov_b32_dpp v45, v29 row_mirror row_mask:0xf bank_mask:0xf
	v_mov_b32_dpp v44, v28 row_mirror row_mask:0xf bank_mask:0xf
	s_waitcnt lgkmcnt(0)
	v_pk_add_f32 v[28:29], v[28:29], v[44:45]
	ds_bpermute_b32 v45, v1, v29
	ds_bpermute_b32 v44, v1, v28
	s_waitcnt lgkmcnt(0)
	v_pk_add_f32 v[28:29], v[28:29], v[44:45]
	s_nop 0
	v_pk_fma_f32 v[28:29], v[28:29], s[8:9], v[122:123] op_sel_hi:[1,0,0]
	v_mov_b32_e32 v45, v30
	v_mul_f32_e32 v44, 0x4b800000, v29
	v_cmp_gt_f32_e64 s[38:39], s66, v29
	v_cmp_gt_f32_e32 vcc, s66, v28
	v_mov_b32_e32 v30, v15
	v_cndmask_b32_e64 v29, v29, v44, s[38:39]
	v_rsq_f32_e32 v29, v29
	s_nop 0
	v_mul_f32_e32 v44, 0x45800000, v29
	v_cndmask_b32_e64 v29, v29, v44, s[38:39]
	v_mul_f32_e32 v120, v69, v29
	v_mul_f32_e32 v29, 0x4b800000, v28
	v_cndmask_b32_e32 v28, v28, v29, vcc
	v_rsq_f32_e32 v28, v28
	v_mov_b32_e32 v44, v14
	v_mul_f32_e32 v29, 0x45800000, v28
	v_cndmask_b32_e32 v28, v28, v29, vcc
	v_mul_f32_e32 v118, v69, v28
	ds_read2_b32 v[28:29], v71 offset1:32
	s_waitcnt lgkmcnt(0)
	v_pk_mul_f32 v[28:29], v[116:117], v[28:29] op_sel_hi:[0,1]
	v_pk_fma_f32 v[44:45], v[44:45], v[114:115], v[28:29] op_sel_hi:[1,0,1] neg_lo:[0,0,1] neg_hi:[0,0,1]
	ds_read2_b32 v[28:29], v71 offset0:64 offset1:96
	v_pk_mul_f32 v[128:129], v[44:45], v[44:45]
	s_waitcnt lgkmcnt(0)
	v_pk_mul_f32 v[28:29], v[116:117], v[28:29] op_sel_hi:[0,1]
	v_pk_fma_f32 v[28:29], v[60:61], v[114:115], v[28:29] op_sel_hi:[1,0,1] neg_lo:[0,0,1] neg_hi:[0,0,1]
	ds_read2_b32 v[60:61], v71 offset0:128 offset1:160
	v_pk_mul_f32 v[130:131], v[28:29], v[28:29]
	s_waitcnt lgkmcnt(0)
	v_pk_mul_f32 v[14:15], v[116:117], v[60:61] op_sel_hi:[0,1]
	v_pk_fma_f32 v[60:61], v[30:31], v[112:113], v[14:15] op_sel_hi:[1,0,1] neg_lo:[0,0,1] neg_hi:[0,0,1]
	ds_read2_b32 v[14:15], v71 offset0:192 offset1:224
	v_pk_mul_f32 v[30:31], v[60:61], v[60:61]
	v_mov_b32_e32 v71, v0
	s_waitcnt lgkmcnt(0)
	v_pk_mul_f32 v[14:15], v[116:117], v[14:15] op_sel_hi:[0,1]
	v_pk_fma_f32 v[14:15], v[62:63], v[112:113], v[14:15] op_sel_hi:[1,0,1] neg_lo:[0,0,1] neg_hi:[0,0,1]
	v_mov_b32_e32 v62, v30
	v_pk_mul_f32 v[46:47], v[14:15], v[14:15]
	v_mov_b32_e32 v63, v128
	v_mov_b32_e32 v128, v31
	v_pk_add_f32 v[30:31], v[62:63], v[128:129]
	v_mov_b32_e32 v62, v46
	v_mov_b32_e32 v63, v130
	v_pk_add_f32 v[30:31], v[30:31], v[62:63]
	v_mov_b32_e32 v130, v47
	v_pk_add_f32 v[30:31], v[30:31], v[130:131]
	s_nop 1
	v_mov_b32_dpp v47, v31 quad_perm:[1,0,3,2] row_mask:0xf bank_mask:0xf
	v_mov_b32_dpp v46, v30 quad_perm:[1,0,3,2] row_mask:0xf bank_mask:0xf
	ds_read2_b32 v[130:131], v67 offset0:128 offset1:160
	v_mov_b32_e32 v128, v48
	v_mov_b32_e32 v129, v64
	v_mov_b32_e32 v64, v49
	s_waitcnt lgkmcnt(0)
	v_pk_add_f32 v[30:31], v[30:31], v[46:47]
	s_nop 1
	v_mov_b32_dpp v47, v31 quad_perm:[2,3,0,1] row_mask:0xf bank_mask:0xf
	v_mov_b32_dpp v46, v30 quad_perm:[2,3,0,1] row_mask:0xf bank_mask:0xf
	s_waitcnt lgkmcnt(0)
	v_pk_add_f32 v[30:31], v[30:31], v[46:47]
	s_nop 1
	v_mov_b32_dpp v47, v31 row_half_mirror row_mask:0xf bank_mask:0xf
	v_mov_b32_dpp v46, v30 row_half_mirror row_mask:0xf bank_mask:0xf
	s_waitcnt lgkmcnt(0)
	v_pk_add_f32 v[30:31], v[30:31], v[46:47]
	s_nop 1
	v_mov_b32_dpp v47, v31 row_mirror row_mask:0xf bank_mask:0xf
	v_mov_b32_dpp v46, v30 row_mirror row_mask:0xf bank_mask:0xf
	s_waitcnt lgkmcnt(0)
	v_pk_add_f32 v[30:31], v[30:31], v[46:47]
	ds_bpermute_b32 v47, v1, v31
	ds_bpermute_b32 v46, v1, v30
	s_waitcnt lgkmcnt(0)
	v_pk_add_f32 v[30:31], v[30:31], v[46:47]
	s_nop 0
	v_pk_fma_f32 v[30:31], v[30:31], s[8:9], v[122:123] op_sel_hi:[1,0,0]
	v_mov_b32_e32 v47, v32
	v_mul_f32_e32 v46, 0x4b800000, v31
	v_cmp_gt_f32_e64 s[38:39], s66, v31
	v_cmp_gt_f32_e32 vcc, s66, v30
	v_mov_b32_e32 v32, v17
	v_cndmask_b32_e64 v31, v31, v46, s[38:39]
	v_rsq_f32_e32 v31, v31
	s_nop 0
	v_mul_f32_e32 v46, 0x45800000, v31
	v_cndmask_b32_e64 v31, v31, v46, s[38:39]
	v_mul_f32_e32 v114, v69, v31
	v_mul_f32_e32 v31, 0x4b800000, v30
	v_cndmask_b32_e32 v30, v30, v31, vcc
	v_rsq_f32_e32 v30, v30
	v_mov_b32_e32 v46, v16
	v_pk_mul_f32 v[16:17], v[116:117], v[130:131] op_sel_hi:[0,1]
	v_pk_fma_f32 v[32:33], v[32:33], v[108:109], v[16:17] op_sel_hi:[1,0,1] neg_lo:[0,0,1] neg_hi:[0,0,1]
	v_mul_f32_e32 v31, 0x45800000, v30
	v_cndmask_b32_e32 v30, v30, v31, vcc
	v_mul_f32_e32 v112, v69, v30
	ds_read2_b32 v[30:31], v67 offset1:32
	ds_read2_b32 v[16:17], v67 offset0:192 offset1:224
	v_pk_mul_f32 v[130:131], v[32:33], v[32:33]
	s_waitcnt lgkmcnt(0)
	v_pk_mul_f32 v[30:31], v[116:117], v[30:31] op_sel_hi:[0,1]
	v_pk_fma_f32 v[46:47], v[46:47], v[110:111], v[30:31] op_sel_hi:[1,0,1] neg_lo:[0,0,1] neg_hi:[0,0,1]
	ds_read2_b32 v[30:31], v67 offset0:64 offset1:96
	s_waitcnt lgkmcnt(0)
	v_pk_mul_f32 v[16:17], v[116:117], v[16:17] op_sel_hi:[0,1]
	v_pk_mul_f32 v[62:63], v[46:47], v[46:47]
	v_pk_fma_f32 v[16:17], v[64:65], v[108:109], v[16:17] op_sel_hi:[1,0,1] neg_lo:[0,0,1] neg_hi:[0,0,1]
	v_mov_b32_e32 v64, v130
	s_waitcnt lgkmcnt(0)
	v_pk_mul_f32 v[30:31], v[116:117], v[30:31] op_sel_hi:[0,1]
	v_pk_fma_f32 v[30:31], v[128:129], v[110:111], v[30:31] op_sel_hi:[1,0,1] neg_lo:[0,0,1] neg_hi:[0,0,1]
	v_pk_mul_f32 v[48:49], v[16:17], v[16:17]
	v_pk_mul_f32 v[128:129], v[30:31], v[30:31]
	v_mov_b32_e32 v65, v62
	v_mov_b32_e32 v62, v131
	v_pk_add_f32 v[62:63], v[64:65], v[62:63]
	v_mov_b32_e32 v64, v48
	v_mov_b32_e32 v65, v128
	v_pk_add_f32 v[62:63], v[62:63], v[64:65]
	v_mov_b32_e32 v128, v49
	v_pk_add_f32 v[48:49], v[62:63], v[128:129]
	s_nop 1
	v_mov_b32_dpp v63, v49 quad_perm:[1,0,3,2] row_mask:0xf bank_mask:0xf
	v_mov_b32_dpp v62, v48 quad_perm:[1,0,3,2] row_mask:0xf bank_mask:0xf
	v_mov_b32_e32 v65, v0
	s_waitcnt lgkmcnt(0)
; __device__ __forceinline__ unsigned f2bf(float f) { unsigned u = __builtin_bit_cast(unsigned, f); return (u + 0x7fffu + ((u >> 16) & 1u)) >> 16; }
; __device__ __forceinline__ unsigned char f8_1(float a) { a = fminf(fmaxf(a, -448.f), 448.f); return (unsigned char)(__builtin_amdgcn_cvt_pk_fp8_f32(a, a, 0, false) & 0xff); }
; __device__ __forceinline__ int crow(int r, int hi) { return (r & 3) + 8 * (r >> 2) + 4 * hi; }
; __device__ __forceinline__ void diff_unit(KP Pk, Frame& F, int l, int b, int h, int qrow0, int nkt) {
;     ...
;         for (int r = 0; r < 16; ++r) { float a = 0.f;
; #pragma unroll
;             for (int nb = 0; nb < 4; ++nb) { const float v = O[nb][r] * rlr[r] - lam * ex[crow(r, hi) * 128 + nb * 32 + r32]; O[nb][r] = v; a += v * v; }
;             a += __shfl_xor(a, 1); a += __shfl_xor(a, 2); a += __shfl_xor(a, 4); a += __shfl_xor(a, 8); a += __shfl_xor(a, 16);
;             ssq[r] = rsqrtf(a * (1.f / 128.f) + NORM_EPS) * (1.f - lam_init); }
;         unsigned char* mix = ws + WS_H + ((size_t)(qrow0 + 32 * rb) * D + 1536 + h * 128) * MIXB;
; #pragma unroll
;         for (int nb = 0; nb < 4; ++nb) { const float w = Pk->in[I_DSUB][l * 128 + nb * 32 + r32];
; #pragma unroll
;             for (int r = 0; r < 16; ++r) { const float y = O[nb][r] * ssq[r] * w; const size_t e = (size_t)crow(r, hi) * D + nb * 32 + r32; if (WOUT_F8) mix[e] = f8_1(y); else ((bf16_t*)mix)[e] = (bf16_t)f2bf(y); } }
	v_pk_add_f32 v[48:49], v[48:49], v[62:63]
	s_nop 1
	v_mov_b32_dpp v63, v49 quad_perm:[2,3,0,1] row_mask:0xf bank_mask:0xf
	v_mov_b32_dpp v62, v48 quad_perm:[2,3,0,1] row_mask:0xf bank_mask:0xf
	s_waitcnt lgkmcnt(0)
	v_pk_add_f32 v[48:49], v[48:49], v[62:63]
	s_nop 1
	v_mov_b32_dpp v63, v49 row_half_mirror row_mask:0xf bank_mask:0xf
	v_mov_b32_dpp v62, v48 row_half_mirror row_mask:0xf bank_mask:0xf
	s_waitcnt lgkmcnt(0)
	v_pk_add_f32 v[48:49], v[48:49], v[62:63]
	s_nop 1
	v_mov_b32_dpp v63, v49 row_mirror row_mask:0xf bank_mask:0xf
	v_mov_b32_dpp v62, v48 row_mirror row_mask:0xf bank_mask:0xf
	s_waitcnt lgkmcnt(0)
	v_pk_add_f32 v[48:49], v[48:49], v[62:63]
	ds_bpermute_b32 v63, v1, v49
	ds_bpermute_b32 v62, v1, v48
	s_waitcnt lgkmcnt(0)
	v_pk_add_f32 v[48:49], v[48:49], v[62:63]
	s_nop 0
	v_pk_fma_f32 v[48:49], v[48:49], s[8:9], v[122:123] op_sel_hi:[1,0,0]
	v_mul_f32_e32 v62, v100, v111
	v_mul_f32_e32 v1, 0x4b800000, v49
	v_cmp_gt_f32_e64 s[38:39], s66, v49
	v_cmp_gt_f32_e32 vcc, s66, v48
	s_lshl_b64 s[8:9], s[40:41], 11
	v_cndmask_b32_e64 v1, v49, v1, s[38:39]
	v_rsq_f32_e32 v1, v1
	s_add_u32 s5, s5, s8
	v_readlane_b32 s8, v254, 62
	s_addc_u32 s9, s8, s9
	v_mul_f32_e32 v49, 0x45800000, v1
	v_cndmask_b32_e64 v1, v1, v49, s[38:39]
	v_mul_f32_e32 v108, v69, v1
	v_mul_f32_e32 v1, 0x4b800000, v48
	v_cndmask_b32_e32 v1, v48, v1, vcc
	v_rsq_f32_e32 v1, v1
	s_add_u32 s8, s5, s18
	s_addc_u32 s9, s9, 0
	v_mul_f32_e32 v48, 0x45800000, v1
	v_cndmask_b32_e32 v1, v1, v48, vcc
	v_lshl_or_b32 v48, s4, 7, v104
	v_ashrrev_i32_e32 v49, 31, v48
	v_lshl_add_u64 v[48:49], v[48:49], 2, v[106:107]
	global_load_dword v67, v[48:49], off
	global_load_dword v236, v[48:49], off offset:128
	global_load_dword v250, v[48:49], off offset:256
	global_load_dword v251, v[48:49], off offset:384
	v_mul_f32_e32 v1, v69, v1
	v_lshl_add_u64 v[104:105], s[8:9], 0, v[104:105]
	v_lshl_add_u64 v[92:93], v[104:105], 0, v[92:93]
	v_lshl_add_u64 v[90:91], v[104:105], 0, v[90:91]
	v_lshl_add_u64 v[88:89], v[104:105], 0, v[88:89]
	v_lshl_add_u64 v[86:87], v[104:105], 0, v[86:87]
	v_lshl_add_u64 v[84:85], v[104:105], 0, v[84:85]
	v_lshl_add_u64 v[82:83], v[104:105], 0, v[82:83]
	v_lshl_add_u64 v[80:81], v[104:105], 0, v[80:81]
	v_lshl_add_u64 v[78:79], v[104:105], 0, v[78:79]
	v_lshl_add_u64 v[74:75], v[104:105], 0, v[74:75]
	v_lshl_add_u64 v[72:73], v[104:105], 0, v[72:73]
	v_lshl_add_u64 v[94:95], v[104:105], 0, v[94:95]
	s_waitcnt vmcnt(0)
	v_mul_f32_e32 v64, v62, v67
	v_med3_f32 v64, v64, s83, v238
	v_cvt_pk_fp8_f32 v65, v64, v64
	v_mul_f32_e32 v64, v102, v109
	v_mul_f32_e32 v69, v64, v67
	v_med3_f32 v69, v69, s83, v238
	v_mul_f32_e32 v34, v34, v67
	v_cvt_pk_fp8_f32 v71, v69, v69
	v_med3_f32 v34, v34, s83, v238
	v_mov_b32_e32 v69, v0
	v_mul_f32_e32 v20, v20, v67
	v_cvt_pk_fp8_f32 v69, v34, v34
	v_med3_f32 v20, v20, s83, v238
	v_mov_b32_e32 v34, v0
	v_cvt_pk_fp8_f32 v34, v20, v20
	v_mul_f32_e32 v20, v36, v119
	v_mul_f32_e32 v20, v20, v67
	v_med3_f32 v20, v20, s83, v238
	global_store_byte v[92:93], v34, off
	v_mov_b32_e32 v34, v0
	v_cvt_pk_fp8_f32 v34, v20, v20
	v_mul_f32_e32 v20, v52, v117
	v_mul_f32_e32 v20, v20, v67
	v_med3_f32 v20, v20, s83, v238
	global_store_byte v[90:91], v34, off
	v_mov_b32_e32 v34, v0
	v_cvt_pk_fp8_f32 v34, v20, v20
	v_mul_f32_e32 v20, v38, v125
	v_mul_f32_e32 v20, v20, v67
	v_med3_f32 v20, v20, s83, v238
	global_store_byte v[88:89], v34, off
	v_mov_b32_e32 v34, v0
	v_cvt_pk_fp8_f32 v34, v20, v20
	v_mul_f32_e32 v20, v54, v121
	v_mul_f32_e32 v20, v20, v67
	v_med3_f32 v20, v20, s83, v238
	global_store_byte v[86:87], v34, off
	v_mov_b32_e32 v34, v0
	v_cvt_pk_fp8_f32 v34, v20, v20
	v_mul_f32_e32 v20, v40, v126
	v_mul_f32_e32 v20, v20, v67
	v_med3_f32 v20, v20, s83, v238
	global_store_byte v[84:85], v34, off
	v_mov_b32_e32 v34, v0
	v_cvt_pk_fp8_f32 v34, v20, v20
	v_mul_f32_e32 v20, v56, v124
	v_mul_f32_e32 v20, v20, v67
	v_med3_f32 v20, v20, s83, v238
	global_store_byte v[82:83], v34, off
	v_mov_b32_e32 v34, v0
	v_cvt_pk_fp8_f32 v34, v20, v20
	v_mul_f32_e32 v20, v42, v120
	v_mul_f32_e32 v20, v20, v67
	v_med3_f32 v20, v20, s83, v238
	global_store_byte v[80:81], v34, off
	v_mov_b32_e32 v34, v0
	v_cvt_pk_fp8_f32 v34, v20, v20
	v_mul_f32_e32 v20, v58, v118
	v_mul_f32_e32 v20, v20, v67
	v_med3_f32 v20, v20, s83, v238
	global_store_byte v[78:79], v34, off
	v_mov_b32_e32 v34, v0
	v_cvt_pk_fp8_f32 v34, v20, v20
	v_mul_f32_e32 v20, v44, v114
	v_mul_f32_e32 v20, v20, v67
	v_med3_f32 v20, v20, s83, v238
	global_store_byte v[74:75], v34, off
	v_mov_b32_e32 v34, v0
	v_cvt_pk_fp8_f32 v34, v20, v20
	v_lshlrev_b64 v[62:63], 11, v[98:99]
	v_mul_f32_e32 v20, v60, v112
	v_lshl_add_u64 v[62:63], v[104:105], 0, v[62:63]
	v_mul_f32_e32 v20, v20, v67
	global_store_byte v[62:63], v65, off
	v_lshlrev_b64 v[64:65], 11, v[96:97]
	global_store_byte v[72:73], v34, off
	v_med3_f32 v20, v20, s83, v238
	v_mov_b32_e32 v34, v0
	v_lshl_add_u64 v[64:65], v[104:105], 0, v[64:65]
	v_cvt_pk_fp8_f32 v34, v20, v20
	global_store_byte v[64:65], v71, off
	v_ashrrev_i32_e32 v71, 31, v70
	v_lshlrev_b64 v[70:71], 11, v[70:71]
	v_mul_f32_e32 v20, v46, v108
	v_lshl_add_u64 v[70:71], v[104:105], 0, v[70:71]
	v_mul_f32_e32 v20, v67, v20
	global_store_byte v[70:71], v34, off
	v_med3_f32 v20, v20, s83, v238
	v_mov_b32_e32 v34, v0
	v_cvt_pk_fp8_f32 v34, v20, v20
	v_mul_f32_e32 v20, v32, v1
	v_mul_f32_e32 v20, v67, v20
	v_med3_f32 v20, v20, s83, v238
	v_mov_b32_e32 v32, v0
	v_cvt_pk_fp8_f32 v32, v20, v20
	global_store_byte v[94:95], v69, off
	v_ashrrev_i32_e32 v69, 31, v68
	v_ashrrev_i32_e32 v67, 31, v66
	v_lshlrev_b64 v[68:69], 11, v[68:69]
	v_lshlrev_b64 v[66:67], 11, v[66:67]
	v_lshl_add_u64 v[68:69], v[104:105], 0, v[68:69]
; __device__ __forceinline__ unsigned f2bf(float f) { unsigned u = __builtin_bit_cast(unsigned, f); return (u + 0x7fffu + ((u >> 16) & 1u)) >> 16; }
; __device__ __forceinline__ unsigned char f8_1(float a) { a = fminf(fmaxf(a, -448.f), 448.f); return (unsigned char)(__builtin_amdgcn_cvt_pk_fp8_f32(a, a, 0, false) & 0xff); }
; __device__ __forceinline__ int crow(int r, int hi) { return (r & 3) + 8 * (r >> 2) + 4 * hi; }
; __device__ __forceinline__ void diff_unit(KP Pk, Frame& F, int l, int b, int h, int qrow0, int nkt) {
;     ...
; #pragma unroll
;         for (int nb = 0; nb < 4; ++nb) { const float w = Pk->in[I_DSUB][l * 128 + nb * 32 + r32];
; #pragma unroll
;             for (int r = 0; r < 16; ++r) { const float y = O[nb][r] * ssq[r] * w; const size_t e = (size_t)crow(r, hi) * D + nb * 32 + r32; if (WOUT_F8) mix[e] = f8_1(y); else ((bf16_t*)mix)[e] = (bf16_t)f2bf(y); } }
	v_lshl_add_u64 v[66:67], v[104:105], 0, v[66:67]
	global_store_byte v[68:69], v34, off
	global_store_byte v[66:67], v32, off
	v_mov_b32_e32 v20, v236
	v_mul_f32_e32 v32, v101, v111
	v_mov_b32_e32 v34, v0
	v_mul_f32_e32 v32, v32, v20
	v_med3_f32 v32, v32, s83, v238
	v_cvt_pk_fp8_f32 v34, v32, v32
	v_mul_f32_e32 v32, v103, v109
	v_mul_f32_e32 v32, v32, v20
	v_med3_f32 v32, v32, s83, v238
	global_store_byte v[62:63], v34, off offset:32
	v_mov_b32_e32 v34, v0
	v_cvt_pk_fp8_f32 v34, v32, v32
	v_mul_f32_e32 v32, v35, v115
	v_mul_f32_e32 v32, v32, v20
	v_med3_f32 v32, v32, s83, v238
	global_store_byte v[64:65], v34, off offset:32
	v_mov_b32_e32 v34, v0
	v_mul_f32_e32 v21, v21, v20
	v_cvt_pk_fp8_f32 v34, v32, v32
	v_med3_f32 v21, v21, s83, v238
	v_mov_b32_e32 v32, v0
	v_cvt_pk_fp8_f32 v32, v21, v21
	v_mul_f32_e32 v21, v37, v119
	v_mul_f32_e32 v21, v21, v20
	v_med3_f32 v21, v21, s83, v238
	global_store_byte v[92:93], v32, off offset:32
	v_mov_b32_e32 v32, v0
	v_cvt_pk_fp8_f32 v32, v21, v21
	v_mul_f32_e32 v21, v53, v117
	v_mul_f32_e32 v21, v21, v20
	v_med3_f32 v21, v21, s83, v238
	global_store_byte v[90:91], v32, off offset:32
	v_mov_b32_e32 v32, v0
	v_cvt_pk_fp8_f32 v32, v21, v21
	v_mul_f32_e32 v21, v39, v125
	v_mul_f32_e32 v21, v21, v20
	v_med3_f32 v21, v21, s83, v238
	global_store_byte v[88:89], v32, off offset:32
	v_mov_b32_e32 v32, v0
	v_cvt_pk_fp8_f32 v32, v21, v21
	v_mul_f32_e32 v21, v55, v121
	v_mul_f32_e32 v21, v21, v20
	v_med3_f32 v21, v21, s83, v238
	global_store_byte v[86:87], v32, off offset:32
	v_mov_b32_e32 v32, v0
	v_cvt_pk_fp8_f32 v32, v21, v21
	v_mul_f32_e32 v21, v41, v126
	v_mul_f32_e32 v21, v21, v20
	v_med3_f32 v21, v21, s83, v238
	global_store_byte v[84:85], v32, off offset:32
	v_mov_b32_e32 v32, v0
	v_cvt_pk_fp8_f32 v32, v21, v21
	v_mul_f32_e32 v21, v57, v124
	v_mul_f32_e32 v21, v21, v20
	v_med3_f32 v21, v21, s83, v238
	global_store_byte v[82:83], v32, off offset:32
	v_mov_b32_e32 v32, v0
	v_cvt_pk_fp8_f32 v32, v21, v21
	v_mul_f32_e32 v21, v43, v120
	v_mul_f32_e32 v21, v21, v20
	v_med3_f32 v21, v21, s83, v238
	global_store_byte v[80:81], v32, off offset:32
	v_mov_b32_e32 v32, v0
	v_cvt_pk_fp8_f32 v32, v21, v21
	v_mul_f32_e32 v21, v59, v118
	v_mul_f32_e32 v21, v21, v20
	v_med3_f32 v21, v21, s83, v238
	global_store_byte v[78:79], v32, off offset:32
	v_mov_b32_e32 v32, v0
	v_cvt_pk_fp8_f32 v32, v21, v21
	v_mul_f32_e32 v21, v45, v114
	v_mul_f32_e32 v21, v21, v20
	v_med3_f32 v21, v21, s83, v238
	global_store_byte v[74:75], v32, off offset:32
	v_mov_b32_e32 v32, v0
	v_cvt_pk_fp8_f32 v32, v21, v21
	v_mul_f32_e32 v21, v61, v112
	v_mul_f32_e32 v21, v21, v20
	v_med3_f32 v21, v21, s83, v238
	global_store_byte v[72:73], v32, off offset:32
	v_mov_b32_e32 v32, v0
	v_cvt_pk_fp8_f32 v32, v21, v21
	v_mul_f32_e32 v21, v47, v108
	v_mul_f32_e32 v21, v21, v20
	v_med3_f32 v21, v21, s83, v238
	global_store_byte v[70:71], v32, off offset:32
	v_mov_b32_e32 v32, v0
	v_cvt_pk_fp8_f32 v32, v21, v21
	v_mul_f32_e32 v21, v33, v1
	v_mul_f32_e32 v20, v21, v20
	v_med3_f32 v20, v20, s83, v238
	v_mov_b32_e32 v21, v0
	v_cvt_pk_fp8_f32 v21, v20, v20
	global_store_byte v[94:95], v34, off offset:32
	global_store_byte v[68:69], v32, off offset:32
	v_mov_b32_e32 v32, v0
	global_store_byte v[66:67], v21, off offset:32
	v_mov_b32_e32 v20, v250
	v_mul_f32_e32 v21, v77, v111
	v_mul_f32_e32 v21, v21, v20
	v_med3_f32 v21, v21, s83, v238
	v_mul_f32_e32 v2, v2, v20
	v_cvt_pk_fp8_f32 v32, v21, v21
	v_med3_f32 v2, v2, s83, v238
	v_mov_b32_e32 v21, v0
	v_cvt_pk_fp8_f32 v21, v2, v2
	v_mul_f32_e32 v2, v18, v115
	v_mul_f32_e32 v2, v2, v20
	v_med3_f32 v2, v2, s83, v238
	v_mov_b32_e32 v18, v0
	v_cvt_pk_fp8_f32 v18, v2, v2
	v_mul_f32_e32 v2, v4, v113
	v_mul_f32_e32 v2, v2, v20
	v_med3_f32 v2, v2, s83, v238
	v_mov_b32_e32 v4, v0
	v_cvt_pk_fp8_f32 v4, v2, v2
	v_mul_f32_e32 v2, v50, v119
	v_mul_f32_e32 v2, v2, v20
	v_med3_f32 v2, v2, s83, v238
	global_store_byte v[92:93], v4, off offset:64
	v_mov_b32_e32 v4, v0
	v_cvt_pk_fp8_f32 v4, v2, v2
	v_mul_f32_e32 v2, v6, v117
	v_mul_f32_e32 v2, v2, v20
	v_med3_f32 v2, v2, s83, v238
	global_store_byte v[90:91], v4, off offset:64
	v_mov_b32_e32 v4, v0
	v_cvt_pk_fp8_f32 v4, v2, v2
	v_mul_f32_e32 v2, v22, v125
	v_mul_f32_e32 v2, v2, v20
	v_med3_f32 v2, v2, s83, v238
	global_store_byte v[88:89], v4, off offset:64
	v_mov_b32_e32 v4, v0
	v_cvt_pk_fp8_f32 v4, v2, v2
	v_mul_f32_e32 v2, v8, v121
	v_mul_f32_e32 v2, v2, v20
	v_med3_f32 v2, v2, s83, v238
	global_store_byte v[86:87], v4, off offset:64
	v_mov_b32_e32 v4, v0
	v_cvt_pk_fp8_f32 v4, v2, v2
	v_mul_f32_e32 v2, v24, v126
; __device__ __forceinline__ unsigned f2bf(float f) { unsigned u = __builtin_bit_cast(unsigned, f); return (u + 0x7fffu + ((u >> 16) & 1u)) >> 16; }
; __device__ __forceinline__ unsigned char f8_1(float a) { a = fminf(fmaxf(a, -448.f), 448.f); return (unsigned char)(__builtin_amdgcn_cvt_pk_fp8_f32(a, a, 0, false) & 0xff); }
; __device__ __forceinline__ int crow(int r, int hi) { return (r & 3) + 8 * (r >> 2) + 4 * hi; }
; __device__ __forceinline__ void diff_unit(KP Pk, Frame& F, int l, int b, int h, int qrow0, int nkt) {
;     ...
; #pragma unroll
;         for (int nb = 0; nb < 4; ++nb) { const float w = Pk->in[I_DSUB][l * 128 + nb * 32 + r32];
; #pragma unroll
;             for (int r = 0; r < 16; ++r) { const float y = O[nb][r] * ssq[r] * w; const size_t e = (size_t)crow(r, hi) * D + nb * 32 + r32; if (WOUT_F8) mix[e] = f8_1(y); else ((bf16_t*)mix)[e] = (bf16_t)f2bf(y); } }
	v_mul_f32_e32 v2, v2, v20
	v_med3_f32 v2, v2, s83, v238
	global_store_byte v[84:85], v4, off offset:64
	v_mov_b32_e32 v4, v0
	v_cvt_pk_fp8_f32 v4, v2, v2
	v_mul_f32_e32 v2, v10, v124
	v_mul_f32_e32 v2, v2, v20
	v_med3_f32 v2, v2, s83, v238
	global_store_byte v[82:83], v4, off offset:64
	v_mov_b32_e32 v4, v0
	v_cvt_pk_fp8_f32 v4, v2, v2
	v_mul_f32_e32 v2, v26, v120
	v_mul_f32_e32 v2, v2, v20
	v_med3_f32 v2, v2, s83, v238
	global_store_byte v[80:81], v4, off offset:64
	v_mov_b32_e32 v4, v0
	v_cvt_pk_fp8_f32 v4, v2, v2
	v_mul_f32_e32 v2, v12, v118
	v_mul_f32_e32 v2, v2, v20
	v_med3_f32 v2, v2, s83, v238
	global_store_byte v[78:79], v4, off offset:64
	v_mov_b32_e32 v4, v0
	v_cvt_pk_fp8_f32 v4, v2, v2
	v_mul_f32_e32 v2, v28, v114
	v_mul_f32_e32 v2, v2, v20
	v_med3_f32 v2, v2, s83, v238
	global_store_byte v[74:75], v4, off offset:64
	v_mov_b32_e32 v4, v0
	v_cvt_pk_fp8_f32 v4, v2, v2
	v_mul_f32_e32 v2, v14, v112
	v_mul_f32_e32 v2, v2, v20
	v_med3_f32 v2, v2, s83, v238
	global_store_byte v[72:73], v4, off offset:64
	v_mov_b32_e32 v4, v0
	v_cvt_pk_fp8_f32 v4, v2, v2
	v_mul_f32_e32 v2, v30, v108
	v_mul_f32_e32 v2, v2, v20
	v_med3_f32 v2, v2, s83, v238
	global_store_byte v[70:71], v4, off offset:64
	v_mov_b32_e32 v4, v0
	v_cvt_pk_fp8_f32 v4, v2, v2
	v_mul_f32_e32 v2, v16, v1
	v_mul_f32_e32 v2, v2, v20
	v_med3_f32 v2, v2, s83, v238
	global_store_byte v[68:69], v4, off offset:64
	v_mov_b32_e32 v4, v0
	v_cvt_pk_fp8_f32 v4, v2, v2
	global_store_byte v[62:63], v32, off offset:64
	global_store_byte v[64:65], v21, off offset:64
	global_store_byte v[94:95], v18, off offset:64
	global_store_byte v[66:67], v4, off offset:64
	v_mov_b32_e32 v2, v251
	v_mul_f32_e32 v4, v76, v111
	v_mov_b32_e32 v6, v0
	v_mul_f32_e32 v1, v17, v1
	v_mul_f32_e32 v4, v4, v2
	v_med3_f32 v4, v4, s83, v238
	v_mul_f32_e32 v3, v3, v2
	v_cvt_pk_fp8_f32 v6, v4, v4
	v_med3_f32 v3, v3, s83, v238
	v_mov_b32_e32 v4, v0
	v_cvt_pk_fp8_f32 v4, v3, v3
	v_mul_f32_e32 v3, v19, v115
	v_mul_f32_e32 v3, v3, v2
	v_med3_f32 v3, v3, s83, v238
	global_store_byte v[64:65], v4, off offset:96
	v_mov_b32_e32 v4, v0
	v_cvt_pk_fp8_f32 v4, v3, v3
	v_mul_f32_e32 v3, v5, v113
	v_mul_f32_e32 v3, v3, v2
	v_med3_f32 v3, v3, s83, v238
	global_store_byte v[94:95], v4, off offset:96
	v_mov_b32_e32 v4, v0
	v_cvt_pk_fp8_f32 v4, v3, v3
	v_mul_f32_e32 v3, v51, v119
	v_mul_f32_e32 v3, v3, v2
	v_med3_f32 v3, v3, s83, v238
	global_store_byte v[92:93], v4, off offset:96
	v_mov_b32_e32 v4, v0
	v_cvt_pk_fp8_f32 v4, v3, v3
	v_mul_f32_e32 v3, v7, v117
	v_mul_f32_e32 v3, v3, v2
	v_med3_f32 v3, v3, s83, v238
	global_store_byte v[90:91], v4, off offset:96
	v_mov_b32_e32 v4, v0
	v_cvt_pk_fp8_f32 v4, v3, v3
	v_mul_f32_e32 v3, v23, v125
	v_mul_f32_e32 v3, v3, v2
	v_med3_f32 v3, v3, s83, v238
	global_store_byte v[88:89], v4, off offset:96
	v_mov_b32_e32 v4, v0
	v_cvt_pk_fp8_f32 v4, v3, v3
	v_mul_f32_e32 v3, v9, v121
	v_mul_f32_e32 v3, v3, v2
	v_med3_f32 v3, v3, s83, v238
	global_store_byte v[86:87], v4, off offset:96
	v_mov_b32_e32 v4, v0
	v_cvt_pk_fp8_f32 v4, v3, v3
	v_mul_f32_e32 v3, v25, v126
	v_mul_f32_e32 v3, v3, v2
	v_med3_f32 v3, v3, s83, v238
	global_store_byte v[84:85], v4, off offset:96
	v_mov_b32_e32 v4, v0
	v_cvt_pk_fp8_f32 v4, v3, v3
	v_mul_f32_e32 v3, v11, v124
	v_mul_f32_e32 v3, v3, v2
	v_med3_f32 v3, v3, s83, v238
	global_store_byte v[82:83], v4, off offset:96
	v_mov_b32_e32 v4, v0
	v_cvt_pk_fp8_f32 v4, v3, v3
	v_mul_f32_e32 v3, v27, v120
	v_mul_f32_e32 v3, v3, v2
	v_med3_f32 v3, v3, s83, v238
	global_store_byte v[80:81], v4, off offset:96
	v_mov_b32_e32 v4, v0
	v_cvt_pk_fp8_f32 v4, v3, v3
	v_mul_f32_e32 v3, v13, v118
	v_mul_f32_e32 v3, v3, v2
	v_med3_f32 v3, v3, s83, v238
	global_store_byte v[78:79], v4, off offset:96
	v_mov_b32_e32 v4, v0
	v_cvt_pk_fp8_f32 v4, v3, v3
	v_mul_f32_e32 v3, v29, v114
	v_mul_f32_e32 v3, v3, v2
	v_med3_f32 v3, v3, s83, v238
	global_store_byte v[74:75], v4, off offset:96
	v_mov_b32_e32 v4, v0
	v_cvt_pk_fp8_f32 v4, v3, v3
	v_mul_f32_e32 v3, v15, v112
	v_mul_f32_e32 v3, v3, v2
	v_med3_f32 v3, v3, s83, v238
	global_store_byte v[72:73], v4, off offset:96
	v_mov_b32_e32 v4, v0
	v_cvt_pk_fp8_f32 v4, v3, v3
	v_mul_f32_e32 v3, v31, v108
	v_mul_f32_e32 v3, v3, v2
	v_mul_f32_e32 v1, v1, v2
	global_store_byte v[70:71], v4, off offset:96
	v_med3_f32 v3, v3, s83, v238
	v_mov_b32_e32 v4, v0
	v_med3_f32 v1, v1, s83, v238
	v_mov_b32_e32 v2, v0
	v_cvt_pk_fp8_f32 v4, v3, v3
	v_cvt_pk_fp8_f32 v2, v1, v1
	global_store_byte v[62:63], v6, off offset:96
	global_store_byte v[68:69], v4, off offset:96
	global_store_byte v[66:67], v2, off offset:96
